# final_d with contiguous tile mapping in the barrier-hosted conversion (each workgroup converts 14 adjacent tiles per barrier)
# speedup vs baseline: 1.0108x; 1.0002x over previous
.Lhw_seam0:
	s_mov_b64 exec, -1
	v_readlane_b32 s2, v239, 0
	s_lshr_b32 s2, s2, 6
	s_sub_i32 s2, s2, 1
	s_mul_i32 s2, s2, 2
	s_add_i32 s2, s2, 0
	s_cmp_gt_u32 s2, 13
	s_cbranch_scc1 .Lhw_seam0_done
	v_readlane_b32 s9, v239, 23
	s_lshr_b32 s9, s9, 3
	s_mul_i32 s9, s9, 14
	s_add_i32 s2, s2, s9
	s_mul_i32 s9, s74, 0
	s_add_i32 s2, s2, s9
	s_cmp_gt_u32 s2, 24575
	s_cbranch_scc1 .Lhw_seam0_done
	v_mbcnt_lo_u32_b32 v178, -1, 0
	v_mbcnt_hi_u32_b32 v178, -1, v178
	v_and_b32_e32 v179, 60, v178
	v_lshlrev_b32_e32 v179, 10, v179
	v_and_b32_e32 v180, 3, v178
	v_lshl_or_b32 v179, v180, 4, v179
	v_add_u32_e32 v180, 0x400, v179
	v_add_u32_e32 v181, 0x800, v179
	v_add_u32_e32 v190, 0xc00, v179
	v_lshlrev_b32_e32 v178, 2, v178
	s_cmp_lt_u32 s2, 16384
	s_cbranch_scc0 .Lhw_dn_s0_0
	s_lshr_b32 s9, s2, 9
	s_bfe_u32 s32, s2, 0x40005
	s_and_b32 s53, s2, 31
	s_lshl_b32 s69, s9, 23
	s_lshl_b32 s100, s32, 19
	s_add_i32 s69, s69, s100
	s_lshl_b32 s100, s53, 8
	s_add_i32 s69, s69, s100
	s_lshl_b32 s98, s9, 11
	s_bfe_u32 s100, s53, 0x30001
	s_lshl_b32 s100, s100, 8
	s_add_i32 s98, s98, s100
	s_lshr_b32 s100, s53, 4
	s_lshl_b32 s100, s100, 7
	s_add_i32 s98, s98, s100
	s_and_b32 s100, s53, 1
	s_lshl_b32 s100, s100, 6
	s_add_i32 s98, s98, s100
	s_lshl_b32 s98, s98, 10
	s_lshl_b32 s100, s32, 6
	s_add_i32 s98, s98, s100
	s_add_i32 s98, s98, 0x2000000
	v_readlane_b32 s82, v239, 11
	v_readlane_b32 s83, v239, 12
	s_movk_i32 s89, 8192
	s_branch .Lhw_go_s0_0

.Lhw_go_s0_0:
	s_add_u32 s100, s82, s69
	s_addc_u32 s101, s83, 0
	v_readlane_b32 s82, v239, 44
	v_readlane_b32 s83, v239, 45
	s_add_u32 s82, s82, s98
	s_addc_u32 s83, s83, 0
	global_load_dword v34, v178, s[100:101] nt
	s_add_u32 s100, s100, s89
	s_addc_u32 s101, s101, 0
	global_load_dword v35, v178, s[100:101] nt
	s_add_u32 s100, s100, s89
	s_addc_u32 s101, s101, 0
	global_load_dword v36, v178, s[100:101] nt
	s_add_u32 s100, s100, s89
	s_addc_u32 s101, s101, 0
	global_load_dword v37, v178, s[100:101] nt
	s_add_u32 s100, s100, s89
	s_addc_u32 s101, s101, 0
	global_load_dword v38, v178, s[100:101] nt
	s_add_u32 s100, s100, s89
	s_addc_u32 s101, s101, 0
	global_load_dword v39, v178, s[100:101] nt
	s_add_u32 s100, s100, s89
	s_addc_u32 s101, s101, 0
	global_load_dword v40, v178, s[100:101] nt
	s_add_u32 s100, s100, s89
	s_addc_u32 s101, s101, 0
	global_load_dword v41, v178, s[100:101] nt
	s_add_u32 s100, s100, s89
	s_addc_u32 s101, s101, 0
	global_load_dword v42, v178, s[100:101] nt
	s_add_u32 s100, s100, s89
	s_addc_u32 s101, s101, 0
	global_load_dword v43, v178, s[100:101] nt
	s_add_u32 s100, s100, s89
	s_addc_u32 s101, s101, 0
	global_load_dword v44, v178, s[100:101] nt
	s_add_u32 s100, s100, s89
	s_addc_u32 s101, s101, 0
	global_load_dword v45, v178, s[100:101] nt
	s_add_u32 s100, s100, s89
	s_addc_u32 s101, s101, 0
	global_load_dword v46, v178, s[100:101] nt
	s_add_u32 s100, s100, s89
	s_addc_u32 s101, s101, 0
	global_load_dword v47, v178, s[100:101] nt
	s_add_u32 s100, s100, s89
	s_addc_u32 s101, s101, 0
	global_load_dword v48, v178, s[100:101] nt
	s_add_u32 s100, s100, s89
	s_addc_u32 s101, s101, 0
	global_load_dword v49, v178, s[100:101] nt
	s_add_u32 s100, s100, s89
	s_addc_u32 s101, s101, 0
	global_load_dword v50, v178, s[100:101] nt
	s_add_u32 s100, s100, s89
	s_addc_u32 s101, s101, 0
	global_load_dword v51, v178, s[100:101] nt
	s_add_u32 s100, s100, s89
	s_addc_u32 s101, s101, 0
	global_load_dword v52, v178, s[100:101] nt
	s_add_u32 s100, s100, s89
	s_addc_u32 s101, s101, 0
	global_load_dword v53, v178, s[100:101] nt
	s_add_u32 s100, s100, s89
	s_addc_u32 s101, s101, 0
	global_load_dword v54, v178, s[100:101] nt
	s_add_u32 s100, s100, s89
	s_addc_u32 s101, s101, 0
	global_load_dword v55, v178, s[100:101] nt
	s_add_u32 s100, s100, s89
	s_addc_u32 s101, s101, 0
	global_load_dword v56, v178, s[100:101] nt
	s_add_u32 s100, s100, s89
	s_addc_u32 s101, s101, 0
	global_load_dword v57, v178, s[100:101] nt
	s_add_u32 s100, s100, s89
	s_addc_u32 s101, s101, 0
	global_load_dword v58, v178, s[100:101] nt
	s_add_u32 s100, s100, s89
	s_addc_u32 s101, s101, 0
	global_load_dword v59, v178, s[100:101] nt
	s_add_u32 s100, s100, s89
	s_addc_u32 s101, s101, 0
	global_load_dword v60, v178, s[100:101] nt
	s_add_u32 s100, s100, s89
	s_addc_u32 s101, s101, 0
	global_load_dword v61, v178, s[100:101] nt
	s_add_u32 s100, s100, s89
	s_addc_u32 s101, s101, 0
	global_load_dword v62, v178, s[100:101] nt
	s_add_u32 s100, s100, s89
	s_addc_u32 s101, s101, 0
	global_load_dword v63, v178, s[100:101] nt
	s_add_u32 s100, s100, s89
	s_addc_u32 s101, s101, 0
	global_load_dword v64, v178, s[100:101] nt
	s_add_u32 s100, s100, s89
	s_addc_u32 s101, s101, 0
	global_load_dword v65, v178, s[100:101] nt
	s_add_u32 s100, s100, s89
	s_addc_u32 s101, s101, 0
	global_load_dword v66, v178, s[100:101] nt
	s_add_u32 s100, s100, s89
	s_addc_u32 s101, s101, 0
	global_load_dword v67, v178, s[100:101] nt
	s_add_u32 s100, s100, s89
	s_addc_u32 s101, s101, 0
	global_load_dword v68, v178, s[100:101] nt
	s_add_u32 s100, s100, s89
	s_addc_u32 s101, s101, 0
	global_load_dword v69, v178, s[100:101] nt
	s_add_u32 s100, s100, s89
	s_addc_u32 s101, s101, 0
	global_load_dword v70, v178, s[100:101] nt
	s_add_u32 s100, s100, s89
	s_addc_u32 s101, s101, 0
	global_load_dword v71, v178, s[100:101] nt
	s_add_u32 s100, s100, s89
	s_addc_u32 s101, s101, 0
	global_load_dword v72, v178, s[100:101] nt
	s_add_u32 s100, s100, s89
	s_addc_u32 s101, s101, 0
	global_load_dword v73, v178, s[100:101] nt
	s_add_u32 s100, s100, s89
	s_addc_u32 s101, s101, 0
	global_load_dword v74, v178, s[100:101] nt
	s_add_u32 s100, s100, s89
	s_addc_u32 s101, s101, 0
	global_load_dword v75, v178, s[100:101] nt
	s_add_u32 s100, s100, s89
	s_addc_u32 s101, s101, 0
	global_load_dword v76, v178, s[100:101] nt
	s_add_u32 s100, s100, s89
	s_addc_u32 s101, s101, 0
	global_load_dword v77, v178, s[100:101] nt
	s_add_u32 s100, s100, s89
	s_addc_u32 s101, s101, 0
	global_load_dword v78, v178, s[100:101] nt
	s_add_u32 s100, s100, s89
	s_addc_u32 s101, s101, 0
	global_load_dword v79, v178, s[100:101] nt
	s_add_u32 s100, s100, s89
	s_addc_u32 s101, s101, 0
	global_load_dword v80, v178, s[100:101] nt
	s_add_u32 s100, s100, s89
	s_addc_u32 s101, s101, 0
	global_load_dword v81, v178, s[100:101] nt
	s_add_u32 s100, s100, s89
	s_addc_u32 s101, s101, 0
	global_load_dword v82, v178, s[100:101] nt
	s_add_u32 s100, s100, s89
	s_addc_u32 s101, s101, 0
	global_load_dword v83, v178, s[100:101] nt
	s_add_u32 s100, s100, s89
	s_addc_u32 s101, s101, 0
	global_load_dword v84, v178, s[100:101] nt
	s_add_u32 s100, s100, s89
	s_addc_u32 s101, s101, 0
	global_load_dword v85, v178, s[100:101] nt
	s_add_u32 s100, s100, s89
	s_addc_u32 s101, s101, 0
	global_load_dword v86, v178, s[100:101] nt
	s_add_u32 s100, s100, s89
	s_addc_u32 s101, s101, 0
	global_load_dword v87, v178, s[100:101] nt
	s_add_u32 s100, s100, s89
	s_addc_u32 s101, s101, 0
	global_load_dword v88, v178, s[100:101] nt
	s_add_u32 s100, s100, s89
	s_addc_u32 s101, s101, 0
	global_load_dword v89, v178, s[100:101] nt
	s_add_u32 s100, s100, s89
	s_addc_u32 s101, s101, 0
	global_load_dword v90, v178, s[100:101] nt
	s_add_u32 s100, s100, s89
	s_addc_u32 s101, s101, 0
	global_load_dword v91, v178, s[100:101] nt
	s_add_u32 s100, s100, s89
	s_addc_u32 s101, s101, 0
	global_load_dword v92, v178, s[100:101] nt
	s_add_u32 s100, s100, s89
	s_addc_u32 s101, s101, 0
	global_load_dword v93, v178, s[100:101] nt
	s_add_u32 s100, s100, s89
	s_addc_u32 s101, s101, 0
	global_load_dword v94, v178, s[100:101] nt
	s_add_u32 s100, s100, s89
	s_addc_u32 s101, s101, 0
	global_load_dword v95, v178, s[100:101] nt
	s_add_u32 s100, s100, s89
	s_addc_u32 s101, s101, 0
	global_load_dword v96, v178, s[100:101] nt
	s_add_u32 s100, s100, s89
	s_addc_u32 s101, s101, 0
	global_load_dword v97, v178, s[100:101] nt
	s_add_u32 s100, s100, s89
	s_addc_u32 s101, s101, 0
	s_waitcnt vmcnt(48)
	v_mul_f32_e32 v34, 0x42000000, v34
	v_mul_f32_e32 v35, 0x42000000, v35
	v_mul_f32_e32 v36, 0x42000000, v36
	v_mul_f32_e32 v37, 0x42000000, v37
	v_mul_f32_e32 v38, 0x42000000, v38
	v_mul_f32_e32 v39, 0x42000000, v39
	v_mul_f32_e32 v40, 0x42000000, v40
	v_mul_f32_e32 v41, 0x42000000, v41
	v_mul_f32_e32 v42, 0x42000000, v42
	v_mul_f32_e32 v43, 0x42000000, v43
	v_mul_f32_e32 v44, 0x42000000, v44
	v_mul_f32_e32 v45, 0x42000000, v45
	v_mul_f32_e32 v46, 0x42000000, v46
	v_mul_f32_e32 v47, 0x42000000, v47
	v_mul_f32_e32 v48, 0x42000000, v48
	v_mul_f32_e32 v49, 0x42000000, v49
	v_cvt_pk_fp8_f32 v154, v34, v35
	v_cvt_pk_fp8_f32 v155, v38, v39
	v_cvt_pk_fp8_f32 v156, v42, v43
	v_cvt_pk_fp8_f32 v157, v46, v47
	v_cvt_pk_fp8_f32 v154, v36, v37 op_sel:[0,0,1]
	v_cvt_pk_fp8_f32 v155, v40, v41 op_sel:[0,0,1]
	v_cvt_pk_fp8_f32 v156, v44, v45 op_sel:[0,0,1]
	v_cvt_pk_fp8_f32 v157, v48, v49 op_sel:[0,0,1]
	s_waitcnt vmcnt(32)
	v_mul_f32_e32 v50, 0x42000000, v50
	v_mul_f32_e32 v51, 0x42000000, v51
	v_mul_f32_e32 v52, 0x42000000, v52
	v_mul_f32_e32 v53, 0x42000000, v53
	v_mul_f32_e32 v54, 0x42000000, v54
	v_mul_f32_e32 v55, 0x42000000, v55
	v_mul_f32_e32 v56, 0x42000000, v56
	v_mul_f32_e32 v57, 0x42000000, v57
	v_mul_f32_e32 v58, 0x42000000, v58
	v_mul_f32_e32 v59, 0x42000000, v59
	v_mul_f32_e32 v60, 0x42000000, v60
	v_mul_f32_e32 v61, 0x42000000, v61
	v_mul_f32_e32 v62, 0x42000000, v62
	v_mul_f32_e32 v63, 0x42000000, v63
	v_mul_f32_e32 v64, 0x42000000, v64
	v_mul_f32_e32 v65, 0x42000000, v65
	v_cvt_pk_fp8_f32 v158, v50, v51
	v_cvt_pk_fp8_f32 v159, v54, v55
	v_cvt_pk_fp8_f32 v160, v58, v59
	v_cvt_pk_fp8_f32 v161, v62, v63
	v_cvt_pk_fp8_f32 v158, v52, v53 op_sel:[0,0,1]
	v_cvt_pk_fp8_f32 v159, v56, v57 op_sel:[0,0,1]
	v_cvt_pk_fp8_f32 v160, v60, v61 op_sel:[0,0,1]
	v_cvt_pk_fp8_f32 v161, v64, v65 op_sel:[0,0,1]
	s_waitcnt vmcnt(16)
	v_mul_f32_e32 v66, 0x42000000, v66
	v_mul_f32_e32 v67, 0x42000000, v67
	v_mul_f32_e32 v68, 0x42000000, v68
	v_mul_f32_e32 v69, 0x42000000, v69
	v_mul_f32_e32 v70, 0x42000000, v70
	v_mul_f32_e32 v71, 0x42000000, v71
	v_mul_f32_e32 v72, 0x42000000, v72
	v_mul_f32_e32 v73, 0x42000000, v73
	v_mul_f32_e32 v74, 0x42000000, v74
	v_mul_f32_e32 v75, 0x42000000, v75
	v_mul_f32_e32 v76, 0x42000000, v76
	v_mul_f32_e32 v77, 0x42000000, v77
	v_mul_f32_e32 v78, 0x42000000, v78
	v_mul_f32_e32 v79, 0x42000000, v79
	v_mul_f32_e32 v80, 0x42000000, v80
	v_mul_f32_e32 v81, 0x42000000, v81
	v_cvt_pk_fp8_f32 v162, v66, v67
	v_cvt_pk_fp8_f32 v163, v70, v71
	v_cvt_pk_fp8_f32 v164, v74, v75
	v_cvt_pk_fp8_f32 v165, v78, v79
	v_cvt_pk_fp8_f32 v162, v68, v69 op_sel:[0,0,1]
	v_cvt_pk_fp8_f32 v163, v72, v73 op_sel:[0,0,1]
	v_cvt_pk_fp8_f32 v164, v76, v77 op_sel:[0,0,1]
	v_cvt_pk_fp8_f32 v165, v80, v81 op_sel:[0,0,1]
	s_waitcnt vmcnt(0)
	v_mul_f32_e32 v82, 0x42000000, v82
	v_mul_f32_e32 v83, 0x42000000, v83
	v_mul_f32_e32 v84, 0x42000000, v84
	v_mul_f32_e32 v85, 0x42000000, v85
	v_mul_f32_e32 v86, 0x42000000, v86
	v_mul_f32_e32 v87, 0x42000000, v87
	v_mul_f32_e32 v88, 0x42000000, v88
	v_mul_f32_e32 v89, 0x42000000, v89
	v_mul_f32_e32 v90, 0x42000000, v90
	v_mul_f32_e32 v91, 0x42000000, v91
	v_mul_f32_e32 v92, 0x42000000, v92
	v_mul_f32_e32 v93, 0x42000000, v93
	v_mul_f32_e32 v94, 0x42000000, v94
	v_mul_f32_e32 v95, 0x42000000, v95
	v_mul_f32_e32 v96, 0x42000000, v96
	v_mul_f32_e32 v97, 0x42000000, v97
	v_cvt_pk_fp8_f32 v166, v82, v83
	v_cvt_pk_fp8_f32 v167, v86, v87
	v_cvt_pk_fp8_f32 v168, v90, v91
	v_cvt_pk_fp8_f32 v169, v94, v95
	v_cvt_pk_fp8_f32 v166, v84, v85 op_sel:[0,0,1]
	v_cvt_pk_fp8_f32 v167, v88, v89 op_sel:[0,0,1]
	v_cvt_pk_fp8_f32 v168, v92, v93 op_sel:[0,0,1]
	v_cvt_pk_fp8_f32 v169, v96, v97 op_sel:[0,0,1]
	s_mov_b32 vcc_lo, 0xaaaaaaaa
	s_mov_b32 vcc_hi, 0xaaaaaaaa
	s_nop 1
	v_cndmask_b32_dpp v170, v154, v158, vcc quad_perm:[1,0,3,2] row_mask:0xf bank_mask:0xf
	v_cndmask_b32_dpp v174, v162, v166, vcc quad_perm:[1,0,3,2] row_mask:0xf bank_mask:0xf
	v_cndmask_b32_dpp v171, v155, v159, vcc quad_perm:[1,0,3,2] row_mask:0xf bank_mask:0xf
	v_cndmask_b32_dpp v175, v163, v167, vcc quad_perm:[1,0,3,2] row_mask:0xf bank_mask:0xf
	v_cndmask_b32_dpp v172, v156, v160, vcc quad_perm:[1,0,3,2] row_mask:0xf bank_mask:0xf
	v_cndmask_b32_dpp v176, v164, v168, vcc quad_perm:[1,0,3,2] row_mask:0xf bank_mask:0xf
	v_cndmask_b32_dpp v173, v157, v161, vcc quad_perm:[1,0,3,2] row_mask:0xf bank_mask:0xf
	v_cndmask_b32_dpp v177, v165, v169, vcc quad_perm:[1,0,3,2] row_mask:0xf bank_mask:0xf
	s_mov_b32 vcc_lo, 0x55555555
	s_mov_b32 vcc_hi, 0x55555555
	s_nop 1
	v_cndmask_b32_dpp v154, v158, v154, vcc quad_perm:[1,0,3,2] row_mask:0xf bank_mask:0xf
	v_cndmask_b32_dpp v162, v166, v162, vcc quad_perm:[1,0,3,2] row_mask:0xf bank_mask:0xf
	v_cndmask_b32_dpp v155, v159, v155, vcc quad_perm:[1,0,3,2] row_mask:0xf bank_mask:0xf
	v_cndmask_b32_dpp v163, v167, v163, vcc quad_perm:[1,0,3,2] row_mask:0xf bank_mask:0xf
	v_cndmask_b32_dpp v156, v160, v156, vcc quad_perm:[1,0,3,2] row_mask:0xf bank_mask:0xf
	v_cndmask_b32_dpp v164, v168, v164, vcc quad_perm:[1,0,3,2] row_mask:0xf bank_mask:0xf
	v_cndmask_b32_dpp v157, v161, v157, vcc quad_perm:[1,0,3,2] row_mask:0xf bank_mask:0xf
	v_cndmask_b32_dpp v165, v169, v165, vcc quad_perm:[1,0,3,2] row_mask:0xf bank_mask:0xf
	s_mov_b32 vcc_lo, 0xcccccccc
	s_mov_b32 vcc_hi, 0xcccccccc
	s_nop 1
	v_cndmask_b32_dpp v158, v154, v162, vcc quad_perm:[2,3,0,1] row_mask:0xf bank_mask:0xf
	v_cndmask_b32_dpp v166, v170, v174, vcc quad_perm:[2,3,0,1] row_mask:0xf bank_mask:0xf
	v_cndmask_b32_dpp v159, v155, v163, vcc quad_perm:[2,3,0,1] row_mask:0xf bank_mask:0xf
	v_cndmask_b32_dpp v167, v171, v175, vcc quad_perm:[2,3,0,1] row_mask:0xf bank_mask:0xf
	v_cndmask_b32_dpp v160, v156, v164, vcc quad_perm:[2,3,0,1] row_mask:0xf bank_mask:0xf
	v_cndmask_b32_dpp v168, v172, v176, vcc quad_perm:[2,3,0,1] row_mask:0xf bank_mask:0xf
	v_cndmask_b32_dpp v161, v157, v165, vcc quad_perm:[2,3,0,1] row_mask:0xf bank_mask:0xf
	v_cndmask_b32_dpp v169, v173, v177, vcc quad_perm:[2,3,0,1] row_mask:0xf bank_mask:0xf
	s_mov_b32 vcc_lo, 0x33333333
	s_mov_b32 vcc_hi, 0x33333333
	s_nop 1
	v_cndmask_b32_dpp v154, v162, v154, vcc quad_perm:[2,3,0,1] row_mask:0xf bank_mask:0xf
	v_cndmask_b32_dpp v170, v174, v170, vcc quad_perm:[2,3,0,1] row_mask:0xf bank_mask:0xf
	v_cndmask_b32_dpp v155, v163, v155, vcc quad_perm:[2,3,0,1] row_mask:0xf bank_mask:0xf
	v_cndmask_b32_dpp v171, v175, v171, vcc quad_perm:[2,3,0,1] row_mask:0xf bank_mask:0xf
	v_cndmask_b32_dpp v156, v164, v156, vcc quad_perm:[2,3,0,1] row_mask:0xf bank_mask:0xf
	v_cndmask_b32_dpp v172, v176, v172, vcc quad_perm:[2,3,0,1] row_mask:0xf bank_mask:0xf
	v_cndmask_b32_dpp v157, v165, v157, vcc quad_perm:[2,3,0,1] row_mask:0xf bank_mask:0xf
	v_cndmask_b32_dpp v173, v177, v173, vcc quad_perm:[2,3,0,1] row_mask:0xf bank_mask:0xf
	global_store_dwordx4 v179, v[154:157], s[82:83] nt
	global_store_dwordx4 v180, v[170:173], s[82:83] nt
	global_store_dwordx4 v181, v[158:161], s[82:83] nt
	global_store_dwordx4 v190, v[166:169], s[82:83] nt
	v_readlane_b32 s2, v239, 0
	s_lshr_b32 s2, s2, 6
	s_sub_i32 s2, s2, 1
	s_mul_i32 s2, s2, 2
	s_add_i32 s2, s2, 1
	s_cmp_gt_u32 s2, 13
	s_cbranch_scc1 .Lhw_seam0_done
	v_readlane_b32 s9, v239, 23
	s_lshr_b32 s9, s9, 3
	s_mul_i32 s9, s9, 14
	s_add_i32 s2, s2, s9
	s_mul_i32 s9, s74, 0
	s_add_i32 s2, s2, s9
	s_cmp_gt_u32 s2, 24575
	s_cbranch_scc1 .Lhw_seam0_done
	v_mbcnt_lo_u32_b32 v178, -1, 0
	v_mbcnt_hi_u32_b32 v178, -1, v178
	v_and_b32_e32 v179, 60, v178
	v_lshlrev_b32_e32 v179, 10, v179
	v_and_b32_e32 v180, 3, v178
	v_lshl_or_b32 v179, v180, 4, v179
	v_add_u32_e32 v180, 0x400, v179
	v_add_u32_e32 v181, 0x800, v179
	v_add_u32_e32 v190, 0xc00, v179
	v_lshlrev_b32_e32 v178, 2, v178
	s_cmp_lt_u32 s2, 16384
	s_cbranch_scc0 .Lhw_dn_s0_1
	s_lshr_b32 s9, s2, 9
	s_bfe_u32 s32, s2, 0x40005
	s_and_b32 s53, s2, 31
	s_lshl_b32 s69, s9, 23
	s_lshl_b32 s100, s32, 19
	s_add_i32 s69, s69, s100
	s_lshl_b32 s100, s53, 8
	s_add_i32 s69, s69, s100
	s_lshl_b32 s98, s9, 11
	s_bfe_u32 s100, s53, 0x30001
	s_lshl_b32 s100, s100, 8
	s_add_i32 s98, s98, s100
	s_lshr_b32 s100, s53, 4
	s_lshl_b32 s100, s100, 7
	s_add_i32 s98, s98, s100
	s_and_b32 s100, s53, 1
	s_lshl_b32 s100, s100, 6
	s_add_i32 s98, s98, s100
	s_lshl_b32 s98, s98, 10
	s_lshl_b32 s100, s32, 6
	s_add_i32 s98, s98, s100
	s_add_i32 s98, s98, 0x2000000
	v_readlane_b32 s82, v239, 11
	v_readlane_b32 s83, v239, 12
	s_movk_i32 s89, 8192
	s_branch .Lhw_go_s0_1

.Lhw_seam1:
	s_mov_b64 exec, -1
	v_readlane_b32 s2, v239, 0
	s_lshr_b32 s2, s2, 6
	s_sub_i32 s2, s2, 1
	s_mul_i32 s2, s2, 2
	s_add_i32 s2, s2, 0
	s_cmp_gt_u32 s2, 13
	s_cbranch_scc1 .Lhw_seam1_done
	v_readlane_b32 s9, v239, 23
	s_lshr_b32 s9, s9, 3
	s_mul_i32 s9, s9, 14
	s_add_i32 s2, s2, s9
	s_mul_i32 s9, s74, 14
	s_add_i32 s2, s2, s9
	s_cmp_gt_u32 s2, 24575
	s_cbranch_scc1 .Lhw_seam1_done
	v_mbcnt_lo_u32_b32 v178, -1, 0
	v_mbcnt_hi_u32_b32 v178, -1, v178
	v_and_b32_e32 v179, 60, v178
	v_lshlrev_b32_e32 v179, 10, v179
	v_and_b32_e32 v180, 3, v178
	v_lshl_or_b32 v179, v180, 4, v179
	v_add_u32_e32 v180, 0x400, v179
	v_add_u32_e32 v181, 0x800, v179
	v_add_u32_e32 v190, 0xc00, v179
	v_lshlrev_b32_e32 v178, 2, v178
	s_cmp_lt_u32 s2, 16384
	s_cbranch_scc0 .Lhw_dn_s1_0
	s_lshr_b32 s9, s2, 9
	s_bfe_u32 s32, s2, 0x40005
	s_and_b32 s53, s2, 31
	s_lshl_b32 s69, s9, 23
	s_lshl_b32 s100, s32, 19
	s_add_i32 s69, s69, s100
	s_lshl_b32 s100, s53, 8
	s_add_i32 s69, s69, s100
	s_lshl_b32 s98, s9, 11
	s_bfe_u32 s100, s53, 0x30001
	s_lshl_b32 s100, s100, 8
	s_add_i32 s98, s98, s100
	s_lshr_b32 s100, s53, 4
	s_lshl_b32 s100, s100, 7
	s_add_i32 s98, s98, s100
	s_and_b32 s100, s53, 1
	s_lshl_b32 s100, s100, 6
	s_add_i32 s98, s98, s100
	s_lshl_b32 s98, s98, 10
	s_lshl_b32 s100, s32, 6
	s_add_i32 s98, s98, s100
	s_add_i32 s98, s98, 0x2000000
	v_readlane_b32 s82, v239, 11
	v_readlane_b32 s83, v239, 12
	s_movk_i32 s89, 8192
	s_branch .Lhw_go_s1_0

.Lhw_go_s1_0:
	s_add_u32 s100, s82, s69
	s_addc_u32 s101, s83, 0
	v_readlane_b32 s82, v239, 44
	v_readlane_b32 s83, v239, 45
	s_add_u32 s82, s82, s98
	s_addc_u32 s83, s83, 0
	global_load_dword v34, v178, s[100:101] nt
	s_add_u32 s100, s100, s89
	s_addc_u32 s101, s101, 0
	global_load_dword v35, v178, s[100:101] nt
	s_add_u32 s100, s100, s89
	s_addc_u32 s101, s101, 0
	global_load_dword v36, v178, s[100:101] nt
	s_add_u32 s100, s100, s89
	s_addc_u32 s101, s101, 0
	global_load_dword v37, v178, s[100:101] nt
	s_add_u32 s100, s100, s89
	s_addc_u32 s101, s101, 0
	global_load_dword v38, v178, s[100:101] nt
	s_add_u32 s100, s100, s89
	s_addc_u32 s101, s101, 0
	global_load_dword v39, v178, s[100:101] nt
	s_add_u32 s100, s100, s89
	s_addc_u32 s101, s101, 0
	global_load_dword v40, v178, s[100:101] nt
	s_add_u32 s100, s100, s89
	s_addc_u32 s101, s101, 0
	global_load_dword v41, v178, s[100:101] nt
	s_add_u32 s100, s100, s89
	s_addc_u32 s101, s101, 0
	global_load_dword v42, v178, s[100:101] nt
	s_add_u32 s100, s100, s89
	s_addc_u32 s101, s101, 0
	global_load_dword v43, v178, s[100:101] nt
	s_add_u32 s100, s100, s89
	s_addc_u32 s101, s101, 0
	global_load_dword v44, v178, s[100:101] nt
	s_add_u32 s100, s100, s89
	s_addc_u32 s101, s101, 0
	global_load_dword v45, v178, s[100:101] nt
	s_add_u32 s100, s100, s89
	s_addc_u32 s101, s101, 0
	global_load_dword v46, v178, s[100:101] nt
	s_add_u32 s100, s100, s89
	s_addc_u32 s101, s101, 0
	global_load_dword v47, v178, s[100:101] nt
	s_add_u32 s100, s100, s89
	s_addc_u32 s101, s101, 0
	global_load_dword v48, v178, s[100:101] nt
	s_add_u32 s100, s100, s89
	s_addc_u32 s101, s101, 0
	global_load_dword v49, v178, s[100:101] nt
	s_add_u32 s100, s100, s89
	s_addc_u32 s101, s101, 0
	global_load_dword v50, v178, s[100:101] nt
	s_add_u32 s100, s100, s89
	s_addc_u32 s101, s101, 0
	global_load_dword v51, v178, s[100:101] nt
	s_add_u32 s100, s100, s89
	s_addc_u32 s101, s101, 0
	global_load_dword v52, v178, s[100:101] nt
	s_add_u32 s100, s100, s89
	s_addc_u32 s101, s101, 0
	global_load_dword v53, v178, s[100:101] nt
	s_add_u32 s100, s100, s89
	s_addc_u32 s101, s101, 0
	global_load_dword v54, v178, s[100:101] nt
	s_add_u32 s100, s100, s89
	s_addc_u32 s101, s101, 0
	global_load_dword v55, v178, s[100:101] nt
	s_add_u32 s100, s100, s89
	s_addc_u32 s101, s101, 0
	global_load_dword v56, v178, s[100:101] nt
	s_add_u32 s100, s100, s89
	s_addc_u32 s101, s101, 0
	global_load_dword v57, v178, s[100:101] nt
	s_add_u32 s100, s100, s89
	s_addc_u32 s101, s101, 0
	global_load_dword v58, v178, s[100:101] nt
	s_add_u32 s100, s100, s89
	s_addc_u32 s101, s101, 0
	global_load_dword v59, v178, s[100:101] nt
	s_add_u32 s100, s100, s89
	s_addc_u32 s101, s101, 0
	global_load_dword v60, v178, s[100:101] nt
	s_add_u32 s100, s100, s89
	s_addc_u32 s101, s101, 0
	global_load_dword v61, v178, s[100:101] nt
	s_add_u32 s100, s100, s89
	s_addc_u32 s101, s101, 0
	global_load_dword v62, v178, s[100:101] nt
	s_add_u32 s100, s100, s89
	s_addc_u32 s101, s101, 0
	global_load_dword v63, v178, s[100:101] nt
	s_add_u32 s100, s100, s89
	s_addc_u32 s101, s101, 0
	global_load_dword v64, v178, s[100:101] nt
	s_add_u32 s100, s100, s89
	s_addc_u32 s101, s101, 0
	global_load_dword v65, v178, s[100:101] nt
	s_add_u32 s100, s100, s89
	s_addc_u32 s101, s101, 0
	global_load_dword v66, v178, s[100:101] nt
	s_add_u32 s100, s100, s89
	s_addc_u32 s101, s101, 0
	global_load_dword v67, v178, s[100:101] nt
	s_add_u32 s100, s100, s89
	s_addc_u32 s101, s101, 0
	global_load_dword v68, v178, s[100:101] nt
	s_add_u32 s100, s100, s89
	s_addc_u32 s101, s101, 0
	global_load_dword v69, v178, s[100:101] nt
	s_add_u32 s100, s100, s89
	s_addc_u32 s101, s101, 0
	global_load_dword v70, v178, s[100:101] nt
	s_add_u32 s100, s100, s89
	s_addc_u32 s101, s101, 0
	global_load_dword v71, v178, s[100:101] nt
	s_add_u32 s100, s100, s89
	s_addc_u32 s101, s101, 0
	global_load_dword v72, v178, s[100:101] nt
	s_add_u32 s100, s100, s89
	s_addc_u32 s101, s101, 0
	global_load_dword v73, v178, s[100:101] nt
	s_add_u32 s100, s100, s89
	s_addc_u32 s101, s101, 0
	global_load_dword v74, v178, s[100:101] nt
	s_add_u32 s100, s100, s89
	s_addc_u32 s101, s101, 0
	global_load_dword v75, v178, s[100:101] nt
	s_add_u32 s100, s100, s89
	s_addc_u32 s101, s101, 0
	global_load_dword v76, v178, s[100:101] nt
	s_add_u32 s100, s100, s89
	s_addc_u32 s101, s101, 0
	global_load_dword v77, v178, s[100:101] nt
	s_add_u32 s100, s100, s89
	s_addc_u32 s101, s101, 0
	global_load_dword v78, v178, s[100:101] nt
	s_add_u32 s100, s100, s89
	s_addc_u32 s101, s101, 0
	global_load_dword v79, v178, s[100:101] nt
	s_add_u32 s100, s100, s89
	s_addc_u32 s101, s101, 0
	global_load_dword v80, v178, s[100:101] nt
	s_add_u32 s100, s100, s89
	s_addc_u32 s101, s101, 0
	global_load_dword v81, v178, s[100:101] nt
	s_add_u32 s100, s100, s89
	s_addc_u32 s101, s101, 0
	global_load_dword v82, v178, s[100:101] nt
	s_add_u32 s100, s100, s89
	s_addc_u32 s101, s101, 0
	global_load_dword v83, v178, s[100:101] nt
	s_add_u32 s100, s100, s89
	s_addc_u32 s101, s101, 0
	global_load_dword v84, v178, s[100:101] nt
	s_add_u32 s100, s100, s89
	s_addc_u32 s101, s101, 0
	global_load_dword v85, v178, s[100:101] nt
	s_add_u32 s100, s100, s89
	s_addc_u32 s101, s101, 0
	global_load_dword v86, v178, s[100:101] nt
	s_add_u32 s100, s100, s89
	s_addc_u32 s101, s101, 0
	global_load_dword v87, v178, s[100:101] nt
	s_add_u32 s100, s100, s89
	s_addc_u32 s101, s101, 0
	global_load_dword v88, v178, s[100:101] nt
	s_add_u32 s100, s100, s89
	s_addc_u32 s101, s101, 0
	global_load_dword v89, v178, s[100:101] nt
	s_add_u32 s100, s100, s89
	s_addc_u32 s101, s101, 0
	global_load_dword v90, v178, s[100:101] nt
	s_add_u32 s100, s100, s89
	s_addc_u32 s101, s101, 0
	global_load_dword v91, v178, s[100:101] nt
	s_add_u32 s100, s100, s89
	s_addc_u32 s101, s101, 0
	global_load_dword v92, v178, s[100:101] nt
	s_add_u32 s100, s100, s89
	s_addc_u32 s101, s101, 0
	global_load_dword v93, v178, s[100:101] nt
	s_add_u32 s100, s100, s89
	s_addc_u32 s101, s101, 0
	global_load_dword v94, v178, s[100:101] nt
	s_add_u32 s100, s100, s89
	s_addc_u32 s101, s101, 0
	global_load_dword v95, v178, s[100:101] nt
	s_add_u32 s100, s100, s89
	s_addc_u32 s101, s101, 0
	global_load_dword v96, v178, s[100:101] nt
	s_add_u32 s100, s100, s89
	s_addc_u32 s101, s101, 0
	global_load_dword v97, v178, s[100:101] nt
	s_add_u32 s100, s100, s89
	s_addc_u32 s101, s101, 0
	s_waitcnt vmcnt(48)
	v_mul_f32_e32 v34, 0x42000000, v34
	v_mul_f32_e32 v35, 0x42000000, v35
	v_mul_f32_e32 v36, 0x42000000, v36
	v_mul_f32_e32 v37, 0x42000000, v37
	v_mul_f32_e32 v38, 0x42000000, v38
	v_mul_f32_e32 v39, 0x42000000, v39
	v_mul_f32_e32 v40, 0x42000000, v40
	v_mul_f32_e32 v41, 0x42000000, v41
	v_mul_f32_e32 v42, 0x42000000, v42
	v_mul_f32_e32 v43, 0x42000000, v43
	v_mul_f32_e32 v44, 0x42000000, v44
	v_mul_f32_e32 v45, 0x42000000, v45
	v_mul_f32_e32 v46, 0x42000000, v46
	v_mul_f32_e32 v47, 0x42000000, v47
	v_mul_f32_e32 v48, 0x42000000, v48
	v_mul_f32_e32 v49, 0x42000000, v49
	v_cvt_pk_fp8_f32 v154, v34, v35
	v_cvt_pk_fp8_f32 v155, v38, v39
	v_cvt_pk_fp8_f32 v156, v42, v43
	v_cvt_pk_fp8_f32 v157, v46, v47
	v_cvt_pk_fp8_f32 v154, v36, v37 op_sel:[0,0,1]
	v_cvt_pk_fp8_f32 v155, v40, v41 op_sel:[0,0,1]
	v_cvt_pk_fp8_f32 v156, v44, v45 op_sel:[0,0,1]
	v_cvt_pk_fp8_f32 v157, v48, v49 op_sel:[0,0,1]
	s_waitcnt vmcnt(32)
	v_mul_f32_e32 v50, 0x42000000, v50
	v_mul_f32_e32 v51, 0x42000000, v51
	v_mul_f32_e32 v52, 0x42000000, v52
	v_mul_f32_e32 v53, 0x42000000, v53
	v_mul_f32_e32 v54, 0x42000000, v54
	v_mul_f32_e32 v55, 0x42000000, v55
	v_mul_f32_e32 v56, 0x42000000, v56
	v_mul_f32_e32 v57, 0x42000000, v57
	v_mul_f32_e32 v58, 0x42000000, v58
	v_mul_f32_e32 v59, 0x42000000, v59
	v_mul_f32_e32 v60, 0x42000000, v60
	v_mul_f32_e32 v61, 0x42000000, v61
	v_mul_f32_e32 v62, 0x42000000, v62
	v_mul_f32_e32 v63, 0x42000000, v63
	v_mul_f32_e32 v64, 0x42000000, v64
	v_mul_f32_e32 v65, 0x42000000, v65
	v_cvt_pk_fp8_f32 v158, v50, v51
	v_cvt_pk_fp8_f32 v159, v54, v55
	v_cvt_pk_fp8_f32 v160, v58, v59
	v_cvt_pk_fp8_f32 v161, v62, v63
	v_cvt_pk_fp8_f32 v158, v52, v53 op_sel:[0,0,1]
	v_cvt_pk_fp8_f32 v159, v56, v57 op_sel:[0,0,1]
	v_cvt_pk_fp8_f32 v160, v60, v61 op_sel:[0,0,1]
	v_cvt_pk_fp8_f32 v161, v64, v65 op_sel:[0,0,1]
	s_waitcnt vmcnt(16)
	v_mul_f32_e32 v66, 0x42000000, v66
	v_mul_f32_e32 v67, 0x42000000, v67
	v_mul_f32_e32 v68, 0x42000000, v68
	v_mul_f32_e32 v69, 0x42000000, v69
	v_mul_f32_e32 v70, 0x42000000, v70
	v_mul_f32_e32 v71, 0x42000000, v71
	v_mul_f32_e32 v72, 0x42000000, v72
	v_mul_f32_e32 v73, 0x42000000, v73
	v_mul_f32_e32 v74, 0x42000000, v74
	v_mul_f32_e32 v75, 0x42000000, v75
	v_mul_f32_e32 v76, 0x42000000, v76
	v_mul_f32_e32 v77, 0x42000000, v77
	v_mul_f32_e32 v78, 0x42000000, v78
	v_mul_f32_e32 v79, 0x42000000, v79
	v_mul_f32_e32 v80, 0x42000000, v80
	v_mul_f32_e32 v81, 0x42000000, v81
	v_cvt_pk_fp8_f32 v162, v66, v67
	v_cvt_pk_fp8_f32 v163, v70, v71
	v_cvt_pk_fp8_f32 v164, v74, v75
	v_cvt_pk_fp8_f32 v165, v78, v79
	v_cvt_pk_fp8_f32 v162, v68, v69 op_sel:[0,0,1]
	v_cvt_pk_fp8_f32 v163, v72, v73 op_sel:[0,0,1]
	v_cvt_pk_fp8_f32 v164, v76, v77 op_sel:[0,0,1]
	v_cvt_pk_fp8_f32 v165, v80, v81 op_sel:[0,0,1]
	s_waitcnt vmcnt(0)
	v_mul_f32_e32 v82, 0x42000000, v82
	v_mul_f32_e32 v83, 0x42000000, v83
	v_mul_f32_e32 v84, 0x42000000, v84
	v_mul_f32_e32 v85, 0x42000000, v85
	v_mul_f32_e32 v86, 0x42000000, v86
	v_mul_f32_e32 v87, 0x42000000, v87
	v_mul_f32_e32 v88, 0x42000000, v88
	v_mul_f32_e32 v89, 0x42000000, v89
	v_mul_f32_e32 v90, 0x42000000, v90
	v_mul_f32_e32 v91, 0x42000000, v91
	v_mul_f32_e32 v92, 0x42000000, v92
	v_mul_f32_e32 v93, 0x42000000, v93
	v_mul_f32_e32 v94, 0x42000000, v94
	v_mul_f32_e32 v95, 0x42000000, v95
	v_mul_f32_e32 v96, 0x42000000, v96
	v_mul_f32_e32 v97, 0x42000000, v97
	v_cvt_pk_fp8_f32 v166, v82, v83
	v_cvt_pk_fp8_f32 v167, v86, v87
	v_cvt_pk_fp8_f32 v168, v90, v91
	v_cvt_pk_fp8_f32 v169, v94, v95
	v_cvt_pk_fp8_f32 v166, v84, v85 op_sel:[0,0,1]
	v_cvt_pk_fp8_f32 v167, v88, v89 op_sel:[0,0,1]
	v_cvt_pk_fp8_f32 v168, v92, v93 op_sel:[0,0,1]
	v_cvt_pk_fp8_f32 v169, v96, v97 op_sel:[0,0,1]
	s_mov_b32 vcc_lo, 0xaaaaaaaa
	s_mov_b32 vcc_hi, 0xaaaaaaaa
	s_nop 1
	v_cndmask_b32_dpp v170, v154, v158, vcc quad_perm:[1,0,3,2] row_mask:0xf bank_mask:0xf
	v_cndmask_b32_dpp v174, v162, v166, vcc quad_perm:[1,0,3,2] row_mask:0xf bank_mask:0xf
	v_cndmask_b32_dpp v171, v155, v159, vcc quad_perm:[1,0,3,2] row_mask:0xf bank_mask:0xf
	v_cndmask_b32_dpp v175, v163, v167, vcc quad_perm:[1,0,3,2] row_mask:0xf bank_mask:0xf
	v_cndmask_b32_dpp v172, v156, v160, vcc quad_perm:[1,0,3,2] row_mask:0xf bank_mask:0xf
	v_cndmask_b32_dpp v176, v164, v168, vcc quad_perm:[1,0,3,2] row_mask:0xf bank_mask:0xf
	v_cndmask_b32_dpp v173, v157, v161, vcc quad_perm:[1,0,3,2] row_mask:0xf bank_mask:0xf
	v_cndmask_b32_dpp v177, v165, v169, vcc quad_perm:[1,0,3,2] row_mask:0xf bank_mask:0xf
	s_mov_b32 vcc_lo, 0x55555555
	s_mov_b32 vcc_hi, 0x55555555
	s_nop 1
	v_cndmask_b32_dpp v154, v158, v154, vcc quad_perm:[1,0,3,2] row_mask:0xf bank_mask:0xf
	v_cndmask_b32_dpp v162, v166, v162, vcc quad_perm:[1,0,3,2] row_mask:0xf bank_mask:0xf
	v_cndmask_b32_dpp v155, v159, v155, vcc quad_perm:[1,0,3,2] row_mask:0xf bank_mask:0xf
	v_cndmask_b32_dpp v163, v167, v163, vcc quad_perm:[1,0,3,2] row_mask:0xf bank_mask:0xf
	v_cndmask_b32_dpp v156, v160, v156, vcc quad_perm:[1,0,3,2] row_mask:0xf bank_mask:0xf
	v_cndmask_b32_dpp v164, v168, v164, vcc quad_perm:[1,0,3,2] row_mask:0xf bank_mask:0xf
	v_cndmask_b32_dpp v157, v161, v157, vcc quad_perm:[1,0,3,2] row_mask:0xf bank_mask:0xf
	v_cndmask_b32_dpp v165, v169, v165, vcc quad_perm:[1,0,3,2] row_mask:0xf bank_mask:0xf
	s_mov_b32 vcc_lo, 0xcccccccc
	s_mov_b32 vcc_hi, 0xcccccccc
	s_nop 1
	v_cndmask_b32_dpp v158, v154, v162, vcc quad_perm:[2,3,0,1] row_mask:0xf bank_mask:0xf
	v_cndmask_b32_dpp v166, v170, v174, vcc quad_perm:[2,3,0,1] row_mask:0xf bank_mask:0xf
	v_cndmask_b32_dpp v159, v155, v163, vcc quad_perm:[2,3,0,1] row_mask:0xf bank_mask:0xf
	v_cndmask_b32_dpp v167, v171, v175, vcc quad_perm:[2,3,0,1] row_mask:0xf bank_mask:0xf
	v_cndmask_b32_dpp v160, v156, v164, vcc quad_perm:[2,3,0,1] row_mask:0xf bank_mask:0xf
	v_cndmask_b32_dpp v168, v172, v176, vcc quad_perm:[2,3,0,1] row_mask:0xf bank_mask:0xf
	v_cndmask_b32_dpp v161, v157, v165, vcc quad_perm:[2,3,0,1] row_mask:0xf bank_mask:0xf
	v_cndmask_b32_dpp v169, v173, v177, vcc quad_perm:[2,3,0,1] row_mask:0xf bank_mask:0xf
	s_mov_b32 vcc_lo, 0x33333333
	s_mov_b32 vcc_hi, 0x33333333
	s_nop 1
	v_cndmask_b32_dpp v154, v162, v154, vcc quad_perm:[2,3,0,1] row_mask:0xf bank_mask:0xf
	v_cndmask_b32_dpp v170, v174, v170, vcc quad_perm:[2,3,0,1] row_mask:0xf bank_mask:0xf
	v_cndmask_b32_dpp v155, v163, v155, vcc quad_perm:[2,3,0,1] row_mask:0xf bank_mask:0xf
	v_cndmask_b32_dpp v171, v175, v171, vcc quad_perm:[2,3,0,1] row_mask:0xf bank_mask:0xf
	v_cndmask_b32_dpp v156, v164, v156, vcc quad_perm:[2,3,0,1] row_mask:0xf bank_mask:0xf
	v_cndmask_b32_dpp v172, v176, v172, vcc quad_perm:[2,3,0,1] row_mask:0xf bank_mask:0xf
	v_cndmask_b32_dpp v157, v165, v157, vcc quad_perm:[2,3,0,1] row_mask:0xf bank_mask:0xf
	v_cndmask_b32_dpp v173, v177, v173, vcc quad_perm:[2,3,0,1] row_mask:0xf bank_mask:0xf
	global_store_dwordx4 v179, v[154:157], s[82:83] nt
	global_store_dwordx4 v180, v[170:173], s[82:83] nt
	global_store_dwordx4 v181, v[158:161], s[82:83] nt
	global_store_dwordx4 v190, v[166:169], s[82:83] nt
	v_readlane_b32 s2, v239, 0
	s_lshr_b32 s2, s2, 6
	s_sub_i32 s2, s2, 1
	s_mul_i32 s2, s2, 2
	s_add_i32 s2, s2, 1
	s_cmp_gt_u32 s2, 13
	s_cbranch_scc1 .Lhw_seam1_done
	v_readlane_b32 s9, v239, 23
	s_lshr_b32 s9, s9, 3
	s_mul_i32 s9, s9, 14
	s_add_i32 s2, s2, s9
	s_mul_i32 s9, s74, 14
	s_add_i32 s2, s2, s9
	s_cmp_gt_u32 s2, 24575
	s_cbranch_scc1 .Lhw_seam1_done
	v_mbcnt_lo_u32_b32 v178, -1, 0
	v_mbcnt_hi_u32_b32 v178, -1, v178
	v_and_b32_e32 v179, 60, v178
	v_lshlrev_b32_e32 v179, 10, v179
	v_and_b32_e32 v180, 3, v178
	v_lshl_or_b32 v179, v180, 4, v179
	v_add_u32_e32 v180, 0x400, v179
	v_add_u32_e32 v181, 0x800, v179
	v_add_u32_e32 v190, 0xc00, v179
	v_lshlrev_b32_e32 v178, 2, v178
	s_cmp_lt_u32 s2, 16384
	s_cbranch_scc0 .Lhw_dn_s1_1
	s_lshr_b32 s9, s2, 9
	s_bfe_u32 s32, s2, 0x40005
	s_and_b32 s53, s2, 31
	s_lshl_b32 s69, s9, 23
	s_lshl_b32 s100, s32, 19
	s_add_i32 s69, s69, s100
	s_lshl_b32 s100, s53, 8
	s_add_i32 s69, s69, s100
	s_lshl_b32 s98, s9, 11
	s_bfe_u32 s100, s53, 0x30001
	s_lshl_b32 s100, s100, 8
	s_add_i32 s98, s98, s100
	s_lshr_b32 s100, s53, 4
	s_lshl_b32 s100, s100, 7
	s_add_i32 s98, s98, s100
	s_and_b32 s100, s53, 1
	s_lshl_b32 s100, s100, 6
	s_add_i32 s98, s98, s100
	s_lshl_b32 s98, s98, 10
	s_lshl_b32 s100, s32, 6
	s_add_i32 s98, s98, s100
	s_add_i32 s98, s98, 0x2000000
	v_readlane_b32 s82, v239, 11
	v_readlane_b32 s83, v239, 12
	s_movk_i32 s89, 8192
	s_branch .Lhw_go_s1_1

.Lhw_seam2:
	s_mov_b64 exec, -1
	v_readlane_b32 s2, v239, 0
	s_lshr_b32 s2, s2, 6
	s_sub_i32 s2, s2, 1
	s_mul_i32 s2, s2, 2
	s_add_i32 s2, s2, 0
	s_cmp_gt_u32 s2, 13
	s_cbranch_scc1 .Lhw_seam2_done
	v_readlane_b32 s9, v239, 23
	s_lshr_b32 s9, s9, 3
	s_mul_i32 s9, s9, 14
	s_add_i32 s2, s2, s9
	s_mul_i32 s9, s74, 28
	s_add_i32 s2, s2, s9
	s_cmp_gt_u32 s2, 24575
	s_cbranch_scc1 .Lhw_seam2_done
	v_mbcnt_lo_u32_b32 v178, -1, 0
	v_mbcnt_hi_u32_b32 v178, -1, v178
	v_and_b32_e32 v179, 60, v178
	v_lshlrev_b32_e32 v179, 10, v179
	v_and_b32_e32 v180, 3, v178
	v_lshl_or_b32 v179, v180, 4, v179
	v_add_u32_e32 v180, 0x400, v179
	v_add_u32_e32 v181, 0x800, v179
	v_add_u32_e32 v190, 0xc00, v179
	v_lshlrev_b32_e32 v178, 2, v178
	s_cmp_lt_u32 s2, 16384
	s_cbranch_scc0 .Lhw_dn_s2_0
	s_lshr_b32 s9, s2, 9
	s_bfe_u32 s32, s2, 0x40005
	s_and_b32 s53, s2, 31
	s_lshl_b32 s69, s9, 23
	s_lshl_b32 s100, s32, 19
	s_add_i32 s69, s69, s100
	s_lshl_b32 s100, s53, 8
	s_add_i32 s69, s69, s100
	s_lshl_b32 s98, s9, 11
	s_bfe_u32 s100, s53, 0x30001
	s_lshl_b32 s100, s100, 8
	s_add_i32 s98, s98, s100
	s_lshr_b32 s100, s53, 4
	s_lshl_b32 s100, s100, 7
	s_add_i32 s98, s98, s100
	s_and_b32 s100, s53, 1
	s_lshl_b32 s100, s100, 6
	s_add_i32 s98, s98, s100
	s_lshl_b32 s98, s98, 10
	s_lshl_b32 s100, s32, 6
	s_add_i32 s98, s98, s100
	s_add_i32 s98, s98, 0x2000000
	v_readlane_b32 s82, v239, 11
	v_readlane_b32 s83, v239, 12
	s_movk_i32 s89, 8192
	s_branch .Lhw_go_s2_0

.Lhw_go_s2_0:
	s_add_u32 s100, s82, s69
	s_addc_u32 s101, s83, 0
	v_readlane_b32 s82, v239, 44
	v_readlane_b32 s83, v239, 45
	s_add_u32 s82, s82, s98
	s_addc_u32 s83, s83, 0
	global_load_dword v34, v178, s[100:101] nt
	s_add_u32 s100, s100, s89
	s_addc_u32 s101, s101, 0
	global_load_dword v35, v178, s[100:101] nt
	s_add_u32 s100, s100, s89
	s_addc_u32 s101, s101, 0
	global_load_dword v36, v178, s[100:101] nt
	s_add_u32 s100, s100, s89
	s_addc_u32 s101, s101, 0
	global_load_dword v37, v178, s[100:101] nt
	s_add_u32 s100, s100, s89
	s_addc_u32 s101, s101, 0
	global_load_dword v38, v178, s[100:101] nt
	s_add_u32 s100, s100, s89
	s_addc_u32 s101, s101, 0
	global_load_dword v39, v178, s[100:101] nt
	s_add_u32 s100, s100, s89
	s_addc_u32 s101, s101, 0
	global_load_dword v40, v178, s[100:101] nt
	s_add_u32 s100, s100, s89
	s_addc_u32 s101, s101, 0
	global_load_dword v41, v178, s[100:101] nt
	s_add_u32 s100, s100, s89
	s_addc_u32 s101, s101, 0
	global_load_dword v42, v178, s[100:101] nt
	s_add_u32 s100, s100, s89
	s_addc_u32 s101, s101, 0
	global_load_dword v43, v178, s[100:101] nt
	s_add_u32 s100, s100, s89
	s_addc_u32 s101, s101, 0
	global_load_dword v44, v178, s[100:101] nt
	s_add_u32 s100, s100, s89
	s_addc_u32 s101, s101, 0
	global_load_dword v45, v178, s[100:101] nt
	s_add_u32 s100, s100, s89
	s_addc_u32 s101, s101, 0
	global_load_dword v46, v178, s[100:101] nt
	s_add_u32 s100, s100, s89
	s_addc_u32 s101, s101, 0
	global_load_dword v47, v178, s[100:101] nt
	s_add_u32 s100, s100, s89
	s_addc_u32 s101, s101, 0
	global_load_dword v48, v178, s[100:101] nt
	s_add_u32 s100, s100, s89
	s_addc_u32 s101, s101, 0
	global_load_dword v49, v178, s[100:101] nt
	s_add_u32 s100, s100, s89
	s_addc_u32 s101, s101, 0
	global_load_dword v50, v178, s[100:101] nt
	s_add_u32 s100, s100, s89
	s_addc_u32 s101, s101, 0
	global_load_dword v51, v178, s[100:101] nt
	s_add_u32 s100, s100, s89
	s_addc_u32 s101, s101, 0
	global_load_dword v52, v178, s[100:101] nt
	s_add_u32 s100, s100, s89
	s_addc_u32 s101, s101, 0
	global_load_dword v53, v178, s[100:101] nt
	s_add_u32 s100, s100, s89
	s_addc_u32 s101, s101, 0
	global_load_dword v54, v178, s[100:101] nt
	s_add_u32 s100, s100, s89
	s_addc_u32 s101, s101, 0
	global_load_dword v55, v178, s[100:101] nt
	s_add_u32 s100, s100, s89
	s_addc_u32 s101, s101, 0
	global_load_dword v56, v178, s[100:101] nt
	s_add_u32 s100, s100, s89
	s_addc_u32 s101, s101, 0
	global_load_dword v57, v178, s[100:101] nt
	s_add_u32 s100, s100, s89
	s_addc_u32 s101, s101, 0
	global_load_dword v58, v178, s[100:101] nt
	s_add_u32 s100, s100, s89
	s_addc_u32 s101, s101, 0
	global_load_dword v59, v178, s[100:101] nt
	s_add_u32 s100, s100, s89
	s_addc_u32 s101, s101, 0
	global_load_dword v60, v178, s[100:101] nt
	s_add_u32 s100, s100, s89
	s_addc_u32 s101, s101, 0
	global_load_dword v61, v178, s[100:101] nt
	s_add_u32 s100, s100, s89
	s_addc_u32 s101, s101, 0
	global_load_dword v62, v178, s[100:101] nt
	s_add_u32 s100, s100, s89
	s_addc_u32 s101, s101, 0
	global_load_dword v63, v178, s[100:101] nt
	s_add_u32 s100, s100, s89
	s_addc_u32 s101, s101, 0
	global_load_dword v64, v178, s[100:101] nt
	s_add_u32 s100, s100, s89
	s_addc_u32 s101, s101, 0
	global_load_dword v65, v178, s[100:101] nt
	s_add_u32 s100, s100, s89
	s_addc_u32 s101, s101, 0
	global_load_dword v66, v178, s[100:101] nt
	s_add_u32 s100, s100, s89
	s_addc_u32 s101, s101, 0
	global_load_dword v67, v178, s[100:101] nt
	s_add_u32 s100, s100, s89
	s_addc_u32 s101, s101, 0
	global_load_dword v68, v178, s[100:101] nt
	s_add_u32 s100, s100, s89
	s_addc_u32 s101, s101, 0
	global_load_dword v69, v178, s[100:101] nt
	s_add_u32 s100, s100, s89
	s_addc_u32 s101, s101, 0
	global_load_dword v70, v178, s[100:101] nt
	s_add_u32 s100, s100, s89
	s_addc_u32 s101, s101, 0
	global_load_dword v71, v178, s[100:101] nt
	s_add_u32 s100, s100, s89
	s_addc_u32 s101, s101, 0
	global_load_dword v72, v178, s[100:101] nt
	s_add_u32 s100, s100, s89
	s_addc_u32 s101, s101, 0
	global_load_dword v73, v178, s[100:101] nt
	s_add_u32 s100, s100, s89
	s_addc_u32 s101, s101, 0
	global_load_dword v74, v178, s[100:101] nt
	s_add_u32 s100, s100, s89
	s_addc_u32 s101, s101, 0
	global_load_dword v75, v178, s[100:101] nt
	s_add_u32 s100, s100, s89
	s_addc_u32 s101, s101, 0
	global_load_dword v76, v178, s[100:101] nt
	s_add_u32 s100, s100, s89
	s_addc_u32 s101, s101, 0
	global_load_dword v77, v178, s[100:101] nt
	s_add_u32 s100, s100, s89
	s_addc_u32 s101, s101, 0
	global_load_dword v78, v178, s[100:101] nt
	s_add_u32 s100, s100, s89
	s_addc_u32 s101, s101, 0
	global_load_dword v79, v178, s[100:101] nt
	s_add_u32 s100, s100, s89
	s_addc_u32 s101, s101, 0
	global_load_dword v80, v178, s[100:101] nt
	s_add_u32 s100, s100, s89
	s_addc_u32 s101, s101, 0
	global_load_dword v81, v178, s[100:101] nt
	s_add_u32 s100, s100, s89
	s_addc_u32 s101, s101, 0
	global_load_dword v82, v178, s[100:101] nt
	s_add_u32 s100, s100, s89
	s_addc_u32 s101, s101, 0
	global_load_dword v83, v178, s[100:101] nt
	s_add_u32 s100, s100, s89
	s_addc_u32 s101, s101, 0
	global_load_dword v84, v178, s[100:101] nt
	s_add_u32 s100, s100, s89
	s_addc_u32 s101, s101, 0
	global_load_dword v85, v178, s[100:101] nt
	s_add_u32 s100, s100, s89
	s_addc_u32 s101, s101, 0
	global_load_dword v86, v178, s[100:101] nt
	s_add_u32 s100, s100, s89
	s_addc_u32 s101, s101, 0
	global_load_dword v87, v178, s[100:101] nt
	s_add_u32 s100, s100, s89
	s_addc_u32 s101, s101, 0
	global_load_dword v88, v178, s[100:101] nt
	s_add_u32 s100, s100, s89
	s_addc_u32 s101, s101, 0
	global_load_dword v89, v178, s[100:101] nt
	s_add_u32 s100, s100, s89
	s_addc_u32 s101, s101, 0
	global_load_dword v90, v178, s[100:101] nt
	s_add_u32 s100, s100, s89
	s_addc_u32 s101, s101, 0
	global_load_dword v91, v178, s[100:101] nt
	s_add_u32 s100, s100, s89
	s_addc_u32 s101, s101, 0
	global_load_dword v92, v178, s[100:101] nt
	s_add_u32 s100, s100, s89
	s_addc_u32 s101, s101, 0
	global_load_dword v93, v178, s[100:101] nt
	s_add_u32 s100, s100, s89
	s_addc_u32 s101, s101, 0
	global_load_dword v94, v178, s[100:101] nt
	s_add_u32 s100, s100, s89
	s_addc_u32 s101, s101, 0
	global_load_dword v95, v178, s[100:101] nt
	s_add_u32 s100, s100, s89
	s_addc_u32 s101, s101, 0
	global_load_dword v96, v178, s[100:101] nt
	s_add_u32 s100, s100, s89
	s_addc_u32 s101, s101, 0
	global_load_dword v97, v178, s[100:101] nt
	s_add_u32 s100, s100, s89
	s_addc_u32 s101, s101, 0
	s_waitcnt vmcnt(48)
	v_mul_f32_e32 v34, 0x42000000, v34
	v_mul_f32_e32 v35, 0x42000000, v35
	v_mul_f32_e32 v36, 0x42000000, v36
	v_mul_f32_e32 v37, 0x42000000, v37
	v_mul_f32_e32 v38, 0x42000000, v38
	v_mul_f32_e32 v39, 0x42000000, v39
	v_mul_f32_e32 v40, 0x42000000, v40
	v_mul_f32_e32 v41, 0x42000000, v41
	v_mul_f32_e32 v42, 0x42000000, v42
	v_mul_f32_e32 v43, 0x42000000, v43
	v_mul_f32_e32 v44, 0x42000000, v44
	v_mul_f32_e32 v45, 0x42000000, v45
	v_mul_f32_e32 v46, 0x42000000, v46
	v_mul_f32_e32 v47, 0x42000000, v47
	v_mul_f32_e32 v48, 0x42000000, v48
	v_mul_f32_e32 v49, 0x42000000, v49
	v_cvt_pk_fp8_f32 v154, v34, v35
	v_cvt_pk_fp8_f32 v155, v38, v39
	v_cvt_pk_fp8_f32 v156, v42, v43
	v_cvt_pk_fp8_f32 v157, v46, v47
	v_cvt_pk_fp8_f32 v154, v36, v37 op_sel:[0,0,1]
	v_cvt_pk_fp8_f32 v155, v40, v41 op_sel:[0,0,1]
	v_cvt_pk_fp8_f32 v156, v44, v45 op_sel:[0,0,1]
	v_cvt_pk_fp8_f32 v157, v48, v49 op_sel:[0,0,1]
	s_waitcnt vmcnt(32)
	v_mul_f32_e32 v50, 0x42000000, v50
	v_mul_f32_e32 v51, 0x42000000, v51
	v_mul_f32_e32 v52, 0x42000000, v52
	v_mul_f32_e32 v53, 0x42000000, v53
	v_mul_f32_e32 v54, 0x42000000, v54
	v_mul_f32_e32 v55, 0x42000000, v55
	v_mul_f32_e32 v56, 0x42000000, v56
	v_mul_f32_e32 v57, 0x42000000, v57
	v_mul_f32_e32 v58, 0x42000000, v58
	v_mul_f32_e32 v59, 0x42000000, v59
	v_mul_f32_e32 v60, 0x42000000, v60
	v_mul_f32_e32 v61, 0x42000000, v61
	v_mul_f32_e32 v62, 0x42000000, v62
	v_mul_f32_e32 v63, 0x42000000, v63
	v_mul_f32_e32 v64, 0x42000000, v64
	v_mul_f32_e32 v65, 0x42000000, v65
	v_cvt_pk_fp8_f32 v158, v50, v51
	v_cvt_pk_fp8_f32 v159, v54, v55
	v_cvt_pk_fp8_f32 v160, v58, v59
	v_cvt_pk_fp8_f32 v161, v62, v63
	v_cvt_pk_fp8_f32 v158, v52, v53 op_sel:[0,0,1]
	v_cvt_pk_fp8_f32 v159, v56, v57 op_sel:[0,0,1]
	v_cvt_pk_fp8_f32 v160, v60, v61 op_sel:[0,0,1]
	v_cvt_pk_fp8_f32 v161, v64, v65 op_sel:[0,0,1]
	s_waitcnt vmcnt(16)
	v_mul_f32_e32 v66, 0x42000000, v66
	v_mul_f32_e32 v67, 0x42000000, v67
	v_mul_f32_e32 v68, 0x42000000, v68
	v_mul_f32_e32 v69, 0x42000000, v69
	v_mul_f32_e32 v70, 0x42000000, v70
	v_mul_f32_e32 v71, 0x42000000, v71
	v_mul_f32_e32 v72, 0x42000000, v72
	v_mul_f32_e32 v73, 0x42000000, v73
	v_mul_f32_e32 v74, 0x42000000, v74
	v_mul_f32_e32 v75, 0x42000000, v75
	v_mul_f32_e32 v76, 0x42000000, v76
	v_mul_f32_e32 v77, 0x42000000, v77
	v_mul_f32_e32 v78, 0x42000000, v78
	v_mul_f32_e32 v79, 0x42000000, v79
	v_mul_f32_e32 v80, 0x42000000, v80
	v_mul_f32_e32 v81, 0x42000000, v81
	v_cvt_pk_fp8_f32 v162, v66, v67
	v_cvt_pk_fp8_f32 v163, v70, v71
	v_cvt_pk_fp8_f32 v164, v74, v75
	v_cvt_pk_fp8_f32 v165, v78, v79
	v_cvt_pk_fp8_f32 v162, v68, v69 op_sel:[0,0,1]
	v_cvt_pk_fp8_f32 v163, v72, v73 op_sel:[0,0,1]
	v_cvt_pk_fp8_f32 v164, v76, v77 op_sel:[0,0,1]
	v_cvt_pk_fp8_f32 v165, v80, v81 op_sel:[0,0,1]
	s_waitcnt vmcnt(0)
	v_mul_f32_e32 v82, 0x42000000, v82
	v_mul_f32_e32 v83, 0x42000000, v83
	v_mul_f32_e32 v84, 0x42000000, v84
	v_mul_f32_e32 v85, 0x42000000, v85
	v_mul_f32_e32 v86, 0x42000000, v86
	v_mul_f32_e32 v87, 0x42000000, v87
	v_mul_f32_e32 v88, 0x42000000, v88
	v_mul_f32_e32 v89, 0x42000000, v89
	v_mul_f32_e32 v90, 0x42000000, v90
	v_mul_f32_e32 v91, 0x42000000, v91
	v_mul_f32_e32 v92, 0x42000000, v92
	v_mul_f32_e32 v93, 0x42000000, v93
	v_mul_f32_e32 v94, 0x42000000, v94
	v_mul_f32_e32 v95, 0x42000000, v95
	v_mul_f32_e32 v96, 0x42000000, v96
	v_mul_f32_e32 v97, 0x42000000, v97
	v_cvt_pk_fp8_f32 v166, v82, v83
	v_cvt_pk_fp8_f32 v167, v86, v87
	v_cvt_pk_fp8_f32 v168, v90, v91
	v_cvt_pk_fp8_f32 v169, v94, v95
	v_cvt_pk_fp8_f32 v166, v84, v85 op_sel:[0,0,1]
	v_cvt_pk_fp8_f32 v167, v88, v89 op_sel:[0,0,1]
	v_cvt_pk_fp8_f32 v168, v92, v93 op_sel:[0,0,1]
	v_cvt_pk_fp8_f32 v169, v96, v97 op_sel:[0,0,1]
	s_mov_b32 vcc_lo, 0xaaaaaaaa
	s_mov_b32 vcc_hi, 0xaaaaaaaa
	s_nop 1
	v_cndmask_b32_dpp v170, v154, v158, vcc quad_perm:[1,0,3,2] row_mask:0xf bank_mask:0xf
	v_cndmask_b32_dpp v174, v162, v166, vcc quad_perm:[1,0,3,2] row_mask:0xf bank_mask:0xf
	v_cndmask_b32_dpp v171, v155, v159, vcc quad_perm:[1,0,3,2] row_mask:0xf bank_mask:0xf
	v_cndmask_b32_dpp v175, v163, v167, vcc quad_perm:[1,0,3,2] row_mask:0xf bank_mask:0xf
	v_cndmask_b32_dpp v172, v156, v160, vcc quad_perm:[1,0,3,2] row_mask:0xf bank_mask:0xf
	v_cndmask_b32_dpp v176, v164, v168, vcc quad_perm:[1,0,3,2] row_mask:0xf bank_mask:0xf
	v_cndmask_b32_dpp v173, v157, v161, vcc quad_perm:[1,0,3,2] row_mask:0xf bank_mask:0xf
	v_cndmask_b32_dpp v177, v165, v169, vcc quad_perm:[1,0,3,2] row_mask:0xf bank_mask:0xf
	s_mov_b32 vcc_lo, 0x55555555
	s_mov_b32 vcc_hi, 0x55555555
	s_nop 1
	v_cndmask_b32_dpp v154, v158, v154, vcc quad_perm:[1,0,3,2] row_mask:0xf bank_mask:0xf
	v_cndmask_b32_dpp v162, v166, v162, vcc quad_perm:[1,0,3,2] row_mask:0xf bank_mask:0xf
	v_cndmask_b32_dpp v155, v159, v155, vcc quad_perm:[1,0,3,2] row_mask:0xf bank_mask:0xf
	v_cndmask_b32_dpp v163, v167, v163, vcc quad_perm:[1,0,3,2] row_mask:0xf bank_mask:0xf
	v_cndmask_b32_dpp v156, v160, v156, vcc quad_perm:[1,0,3,2] row_mask:0xf bank_mask:0xf
	v_cndmask_b32_dpp v164, v168, v164, vcc quad_perm:[1,0,3,2] row_mask:0xf bank_mask:0xf
	v_cndmask_b32_dpp v157, v161, v157, vcc quad_perm:[1,0,3,2] row_mask:0xf bank_mask:0xf
	v_cndmask_b32_dpp v165, v169, v165, vcc quad_perm:[1,0,3,2] row_mask:0xf bank_mask:0xf
	s_mov_b32 vcc_lo, 0xcccccccc
	s_mov_b32 vcc_hi, 0xcccccccc
	s_nop 1
	v_cndmask_b32_dpp v158, v154, v162, vcc quad_perm:[2,3,0,1] row_mask:0xf bank_mask:0xf
	v_cndmask_b32_dpp v166, v170, v174, vcc quad_perm:[2,3,0,1] row_mask:0xf bank_mask:0xf
	v_cndmask_b32_dpp v159, v155, v163, vcc quad_perm:[2,3,0,1] row_mask:0xf bank_mask:0xf
	v_cndmask_b32_dpp v167, v171, v175, vcc quad_perm:[2,3,0,1] row_mask:0xf bank_mask:0xf
	v_cndmask_b32_dpp v160, v156, v164, vcc quad_perm:[2,3,0,1] row_mask:0xf bank_mask:0xf
	v_cndmask_b32_dpp v168, v172, v176, vcc quad_perm:[2,3,0,1] row_mask:0xf bank_mask:0xf
	v_cndmask_b32_dpp v161, v157, v165, vcc quad_perm:[2,3,0,1] row_mask:0xf bank_mask:0xf
	v_cndmask_b32_dpp v169, v173, v177, vcc quad_perm:[2,3,0,1] row_mask:0xf bank_mask:0xf
	s_mov_b32 vcc_lo, 0x33333333
	s_mov_b32 vcc_hi, 0x33333333
	s_nop 1
	v_cndmask_b32_dpp v154, v162, v154, vcc quad_perm:[2,3,0,1] row_mask:0xf bank_mask:0xf
	v_cndmask_b32_dpp v170, v174, v170, vcc quad_perm:[2,3,0,1] row_mask:0xf bank_mask:0xf
	v_cndmask_b32_dpp v155, v163, v155, vcc quad_perm:[2,3,0,1] row_mask:0xf bank_mask:0xf
	v_cndmask_b32_dpp v171, v175, v171, vcc quad_perm:[2,3,0,1] row_mask:0xf bank_mask:0xf
	v_cndmask_b32_dpp v156, v164, v156, vcc quad_perm:[2,3,0,1] row_mask:0xf bank_mask:0xf
	v_cndmask_b32_dpp v172, v176, v172, vcc quad_perm:[2,3,0,1] row_mask:0xf bank_mask:0xf
	v_cndmask_b32_dpp v157, v165, v157, vcc quad_perm:[2,3,0,1] row_mask:0xf bank_mask:0xf
	v_cndmask_b32_dpp v173, v177, v173, vcc quad_perm:[2,3,0,1] row_mask:0xf bank_mask:0xf
	global_store_dwordx4 v179, v[154:157], s[82:83] nt
	global_store_dwordx4 v180, v[170:173], s[82:83] nt
	global_store_dwordx4 v181, v[158:161], s[82:83] nt
	global_store_dwordx4 v190, v[166:169], s[82:83] nt
	v_readlane_b32 s2, v239, 0
	s_lshr_b32 s2, s2, 6
	s_sub_i32 s2, s2, 1
	s_mul_i32 s2, s2, 2
	s_add_i32 s2, s2, 1
	s_cmp_gt_u32 s2, 13
	s_cbranch_scc1 .Lhw_seam2_done
	v_readlane_b32 s9, v239, 23
	s_lshr_b32 s9, s9, 3
	s_mul_i32 s9, s9, 14
	s_add_i32 s2, s2, s9
	s_mul_i32 s9, s74, 28
	s_add_i32 s2, s2, s9
	s_cmp_gt_u32 s2, 24575
	s_cbranch_scc1 .Lhw_seam2_done
	v_mbcnt_lo_u32_b32 v178, -1, 0
	v_mbcnt_hi_u32_b32 v178, -1, v178
	v_and_b32_e32 v179, 60, v178
	v_lshlrev_b32_e32 v179, 10, v179
	v_and_b32_e32 v180, 3, v178
	v_lshl_or_b32 v179, v180, 4, v179
	v_add_u32_e32 v180, 0x400, v179
	v_add_u32_e32 v181, 0x800, v179
	v_add_u32_e32 v190, 0xc00, v179
	v_lshlrev_b32_e32 v178, 2, v178
	s_cmp_lt_u32 s2, 16384
	s_cbranch_scc0 .Lhw_dn_s2_1
	s_lshr_b32 s9, s2, 9
	s_bfe_u32 s32, s2, 0x40005
	s_and_b32 s53, s2, 31
	s_lshl_b32 s69, s9, 23
	s_lshl_b32 s100, s32, 19
	s_add_i32 s69, s69, s100
	s_lshl_b32 s100, s53, 8
	s_add_i32 s69, s69, s100
	s_lshl_b32 s98, s9, 11
	s_bfe_u32 s100, s53, 0x30001
	s_lshl_b32 s100, s100, 8
	s_add_i32 s98, s98, s100
	s_lshr_b32 s100, s53, 4
	s_lshl_b32 s100, s100, 7
	s_add_i32 s98, s98, s100
	s_and_b32 s100, s53, 1
	s_lshl_b32 s100, s100, 6
	s_add_i32 s98, s98, s100
	s_lshl_b32 s98, s98, 10
	s_lshl_b32 s100, s32, 6
	s_add_i32 s98, s98, s100
	s_add_i32 s98, s98, 0x2000000
	v_readlane_b32 s82, v239, 11
	v_readlane_b32 s83, v239, 12
	s_movk_i32 s89, 8192
	s_branch .Lhw_go_s2_1

.Lhw_seam3:
	s_mov_b64 exec, -1
	v_readlane_b32 s2, v239, 0
	s_lshr_b32 s2, s2, 6
	s_sub_i32 s2, s2, 1
	s_mul_i32 s2, s2, 2
	s_add_i32 s2, s2, 0
	s_cmp_gt_u32 s2, 13
	s_cbranch_scc1 .Lhw_seam3_done
	v_readlane_b32 s9, v239, 23
	s_lshr_b32 s9, s9, 3
	s_mul_i32 s9, s9, 14
	s_add_i32 s2, s2, s9
	s_mul_i32 s9, s74, 42
	s_add_i32 s2, s2, s9
	s_cmp_gt_u32 s2, 24575
	s_cbranch_scc1 .Lhw_seam3_done
	v_mbcnt_lo_u32_b32 v178, -1, 0
	v_mbcnt_hi_u32_b32 v178, -1, v178
	v_and_b32_e32 v179, 60, v178
	v_lshlrev_b32_e32 v179, 10, v179
	v_and_b32_e32 v180, 3, v178
	v_lshl_or_b32 v179, v180, 4, v179
	v_add_u32_e32 v180, 0x400, v179
	v_add_u32_e32 v181, 0x800, v179
	v_add_u32_e32 v190, 0xc00, v179
	v_lshlrev_b32_e32 v178, 2, v178
	s_cmp_lt_u32 s2, 16384
	s_cbranch_scc0 .Lhw_dn_s3_0
	s_lshr_b32 s9, s2, 9
	s_bfe_u32 s32, s2, 0x40005
	s_and_b32 s53, s2, 31
	s_lshl_b32 s69, s9, 23
	s_lshl_b32 s100, s32, 19
	s_add_i32 s69, s69, s100
	s_lshl_b32 s100, s53, 8
	s_add_i32 s69, s69, s100
	s_lshl_b32 s98, s9, 11
	s_bfe_u32 s100, s53, 0x30001
	s_lshl_b32 s100, s100, 8
	s_add_i32 s98, s98, s100
	s_lshr_b32 s100, s53, 4
	s_lshl_b32 s100, s100, 7
	s_add_i32 s98, s98, s100
	s_and_b32 s100, s53, 1
	s_lshl_b32 s100, s100, 6
	s_add_i32 s98, s98, s100
	s_lshl_b32 s98, s98, 10
	s_lshl_b32 s100, s32, 6
	s_add_i32 s98, s98, s100
	s_add_i32 s98, s98, 0x2000000
	v_readlane_b32 s82, v239, 11
	v_readlane_b32 s83, v239, 12
	s_movk_i32 s89, 8192
	s_branch .Lhw_go_s3_0

.Lhw_go_s3_0:
	s_add_u32 s100, s82, s69
	s_addc_u32 s101, s83, 0
	v_readlane_b32 s82, v239, 44
	v_readlane_b32 s83, v239, 45
	s_add_u32 s82, s82, s98
	s_addc_u32 s83, s83, 0
	global_load_dword v34, v178, s[100:101] nt
	s_add_u32 s100, s100, s89
	s_addc_u32 s101, s101, 0
	global_load_dword v35, v178, s[100:101] nt
	s_add_u32 s100, s100, s89
	s_addc_u32 s101, s101, 0
	global_load_dword v36, v178, s[100:101] nt
	s_add_u32 s100, s100, s89
	s_addc_u32 s101, s101, 0
	global_load_dword v37, v178, s[100:101] nt
	s_add_u32 s100, s100, s89
	s_addc_u32 s101, s101, 0
	global_load_dword v38, v178, s[100:101] nt
	s_add_u32 s100, s100, s89
	s_addc_u32 s101, s101, 0
	global_load_dword v39, v178, s[100:101] nt
	s_add_u32 s100, s100, s89
	s_addc_u32 s101, s101, 0
	global_load_dword v40, v178, s[100:101] nt
	s_add_u32 s100, s100, s89
	s_addc_u32 s101, s101, 0
	global_load_dword v41, v178, s[100:101] nt
	s_add_u32 s100, s100, s89
	s_addc_u32 s101, s101, 0
	global_load_dword v42, v178, s[100:101] nt
	s_add_u32 s100, s100, s89
	s_addc_u32 s101, s101, 0
	global_load_dword v43, v178, s[100:101] nt
	s_add_u32 s100, s100, s89
	s_addc_u32 s101, s101, 0
	global_load_dword v44, v178, s[100:101] nt
	s_add_u32 s100, s100, s89
	s_addc_u32 s101, s101, 0
	global_load_dword v45, v178, s[100:101] nt
	s_add_u32 s100, s100, s89
	s_addc_u32 s101, s101, 0
	global_load_dword v46, v178, s[100:101] nt
	s_add_u32 s100, s100, s89
	s_addc_u32 s101, s101, 0
	global_load_dword v47, v178, s[100:101] nt
	s_add_u32 s100, s100, s89
	s_addc_u32 s101, s101, 0
	global_load_dword v48, v178, s[100:101] nt
	s_add_u32 s100, s100, s89
	s_addc_u32 s101, s101, 0
	global_load_dword v49, v178, s[100:101] nt
	s_add_u32 s100, s100, s89
	s_addc_u32 s101, s101, 0
	global_load_dword v50, v178, s[100:101] nt
	s_add_u32 s100, s100, s89
	s_addc_u32 s101, s101, 0
	global_load_dword v51, v178, s[100:101] nt
	s_add_u32 s100, s100, s89
	s_addc_u32 s101, s101, 0
	global_load_dword v52, v178, s[100:101] nt
	s_add_u32 s100, s100, s89
	s_addc_u32 s101, s101, 0
	global_load_dword v53, v178, s[100:101] nt
	s_add_u32 s100, s100, s89
	s_addc_u32 s101, s101, 0
	global_load_dword v54, v178, s[100:101] nt
	s_add_u32 s100, s100, s89
	s_addc_u32 s101, s101, 0
	global_load_dword v55, v178, s[100:101] nt
	s_add_u32 s100, s100, s89
	s_addc_u32 s101, s101, 0
	global_load_dword v56, v178, s[100:101] nt
	s_add_u32 s100, s100, s89
	s_addc_u32 s101, s101, 0
	global_load_dword v57, v178, s[100:101] nt
	s_add_u32 s100, s100, s89
	s_addc_u32 s101, s101, 0
	global_load_dword v58, v178, s[100:101] nt
	s_add_u32 s100, s100, s89
	s_addc_u32 s101, s101, 0
	global_load_dword v59, v178, s[100:101] nt
	s_add_u32 s100, s100, s89
	s_addc_u32 s101, s101, 0
	global_load_dword v60, v178, s[100:101] nt
	s_add_u32 s100, s100, s89
	s_addc_u32 s101, s101, 0
	global_load_dword v61, v178, s[100:101] nt
	s_add_u32 s100, s100, s89
	s_addc_u32 s101, s101, 0
	global_load_dword v62, v178, s[100:101] nt
	s_add_u32 s100, s100, s89
	s_addc_u32 s101, s101, 0
	global_load_dword v63, v178, s[100:101] nt
	s_add_u32 s100, s100, s89
	s_addc_u32 s101, s101, 0
	global_load_dword v64, v178, s[100:101] nt
	s_add_u32 s100, s100, s89
	s_addc_u32 s101, s101, 0
	global_load_dword v65, v178, s[100:101] nt
	s_add_u32 s100, s100, s89
	s_addc_u32 s101, s101, 0
	global_load_dword v66, v178, s[100:101] nt
	s_add_u32 s100, s100, s89
	s_addc_u32 s101, s101, 0
	global_load_dword v67, v178, s[100:101] nt
	s_add_u32 s100, s100, s89
	s_addc_u32 s101, s101, 0
	global_load_dword v68, v178, s[100:101] nt
	s_add_u32 s100, s100, s89
	s_addc_u32 s101, s101, 0
	global_load_dword v69, v178, s[100:101] nt
	s_add_u32 s100, s100, s89
	s_addc_u32 s101, s101, 0
	global_load_dword v70, v178, s[100:101] nt
	s_add_u32 s100, s100, s89
	s_addc_u32 s101, s101, 0
	global_load_dword v71, v178, s[100:101] nt
	s_add_u32 s100, s100, s89
	s_addc_u32 s101, s101, 0
	global_load_dword v72, v178, s[100:101] nt
	s_add_u32 s100, s100, s89
	s_addc_u32 s101, s101, 0
	global_load_dword v73, v178, s[100:101] nt
	s_add_u32 s100, s100, s89
	s_addc_u32 s101, s101, 0
	global_load_dword v74, v178, s[100:101] nt
	s_add_u32 s100, s100, s89
	s_addc_u32 s101, s101, 0
	global_load_dword v75, v178, s[100:101] nt
	s_add_u32 s100, s100, s89
	s_addc_u32 s101, s101, 0
	global_load_dword v76, v178, s[100:101] nt
	s_add_u32 s100, s100, s89
	s_addc_u32 s101, s101, 0
	global_load_dword v77, v178, s[100:101] nt
	s_add_u32 s100, s100, s89
	s_addc_u32 s101, s101, 0
	global_load_dword v78, v178, s[100:101] nt
	s_add_u32 s100, s100, s89
	s_addc_u32 s101, s101, 0
	global_load_dword v79, v178, s[100:101] nt
	s_add_u32 s100, s100, s89
	s_addc_u32 s101, s101, 0
	global_load_dword v80, v178, s[100:101] nt
	s_add_u32 s100, s100, s89
	s_addc_u32 s101, s101, 0
	global_load_dword v81, v178, s[100:101] nt
	s_add_u32 s100, s100, s89
	s_addc_u32 s101, s101, 0
	global_load_dword v82, v178, s[100:101] nt
	s_add_u32 s100, s100, s89
	s_addc_u32 s101, s101, 0
	global_load_dword v83, v178, s[100:101] nt
	s_add_u32 s100, s100, s89
	s_addc_u32 s101, s101, 0
	global_load_dword v84, v178, s[100:101] nt
	s_add_u32 s100, s100, s89
	s_addc_u32 s101, s101, 0
	global_load_dword v85, v178, s[100:101] nt
	s_add_u32 s100, s100, s89
	s_addc_u32 s101, s101, 0
	global_load_dword v86, v178, s[100:101] nt
	s_add_u32 s100, s100, s89
	s_addc_u32 s101, s101, 0
	global_load_dword v87, v178, s[100:101] nt
	s_add_u32 s100, s100, s89
	s_addc_u32 s101, s101, 0
	global_load_dword v88, v178, s[100:101] nt
	s_add_u32 s100, s100, s89
	s_addc_u32 s101, s101, 0
	global_load_dword v89, v178, s[100:101] nt
	s_add_u32 s100, s100, s89
	s_addc_u32 s101, s101, 0
	global_load_dword v90, v178, s[100:101] nt
	s_add_u32 s100, s100, s89
	s_addc_u32 s101, s101, 0
	global_load_dword v91, v178, s[100:101] nt
	s_add_u32 s100, s100, s89
	s_addc_u32 s101, s101, 0
	global_load_dword v92, v178, s[100:101] nt
	s_add_u32 s100, s100, s89
	s_addc_u32 s101, s101, 0
	global_load_dword v93, v178, s[100:101] nt
	s_add_u32 s100, s100, s89
	s_addc_u32 s101, s101, 0
	global_load_dword v94, v178, s[100:101] nt
	s_add_u32 s100, s100, s89
	s_addc_u32 s101, s101, 0
	global_load_dword v95, v178, s[100:101] nt
	s_add_u32 s100, s100, s89
	s_addc_u32 s101, s101, 0
	global_load_dword v96, v178, s[100:101] nt
	s_add_u32 s100, s100, s89
	s_addc_u32 s101, s101, 0
	global_load_dword v97, v178, s[100:101] nt
	s_add_u32 s100, s100, s89
	s_addc_u32 s101, s101, 0
	s_waitcnt vmcnt(48)
	v_mul_f32_e32 v34, 0x42000000, v34
	v_mul_f32_e32 v35, 0x42000000, v35
	v_mul_f32_e32 v36, 0x42000000, v36
	v_mul_f32_e32 v37, 0x42000000, v37
	v_mul_f32_e32 v38, 0x42000000, v38
	v_mul_f32_e32 v39, 0x42000000, v39
	v_mul_f32_e32 v40, 0x42000000, v40
	v_mul_f32_e32 v41, 0x42000000, v41
	v_mul_f32_e32 v42, 0x42000000, v42
	v_mul_f32_e32 v43, 0x42000000, v43
	v_mul_f32_e32 v44, 0x42000000, v44
	v_mul_f32_e32 v45, 0x42000000, v45
	v_mul_f32_e32 v46, 0x42000000, v46
	v_mul_f32_e32 v47, 0x42000000, v47
	v_mul_f32_e32 v48, 0x42000000, v48
	v_mul_f32_e32 v49, 0x42000000, v49
	v_cvt_pk_fp8_f32 v154, v34, v35
	v_cvt_pk_fp8_f32 v155, v38, v39
	v_cvt_pk_fp8_f32 v156, v42, v43
	v_cvt_pk_fp8_f32 v157, v46, v47
	v_cvt_pk_fp8_f32 v154, v36, v37 op_sel:[0,0,1]
	v_cvt_pk_fp8_f32 v155, v40, v41 op_sel:[0,0,1]
	v_cvt_pk_fp8_f32 v156, v44, v45 op_sel:[0,0,1]
	v_cvt_pk_fp8_f32 v157, v48, v49 op_sel:[0,0,1]
	s_waitcnt vmcnt(32)
	v_mul_f32_e32 v50, 0x42000000, v50
	v_mul_f32_e32 v51, 0x42000000, v51
	v_mul_f32_e32 v52, 0x42000000, v52
	v_mul_f32_e32 v53, 0x42000000, v53
	v_mul_f32_e32 v54, 0x42000000, v54
	v_mul_f32_e32 v55, 0x42000000, v55
	v_mul_f32_e32 v56, 0x42000000, v56
	v_mul_f32_e32 v57, 0x42000000, v57
	v_mul_f32_e32 v58, 0x42000000, v58
	v_mul_f32_e32 v59, 0x42000000, v59
	v_mul_f32_e32 v60, 0x42000000, v60
	v_mul_f32_e32 v61, 0x42000000, v61
	v_mul_f32_e32 v62, 0x42000000, v62
	v_mul_f32_e32 v63, 0x42000000, v63
	v_mul_f32_e32 v64, 0x42000000, v64
	v_mul_f32_e32 v65, 0x42000000, v65
	v_cvt_pk_fp8_f32 v158, v50, v51
	v_cvt_pk_fp8_f32 v159, v54, v55
	v_cvt_pk_fp8_f32 v160, v58, v59
	v_cvt_pk_fp8_f32 v161, v62, v63
	v_cvt_pk_fp8_f32 v158, v52, v53 op_sel:[0,0,1]
	v_cvt_pk_fp8_f32 v159, v56, v57 op_sel:[0,0,1]
	v_cvt_pk_fp8_f32 v160, v60, v61 op_sel:[0,0,1]
	v_cvt_pk_fp8_f32 v161, v64, v65 op_sel:[0,0,1]
	s_waitcnt vmcnt(16)
	v_mul_f32_e32 v66, 0x42000000, v66
	v_mul_f32_e32 v67, 0x42000000, v67
	v_mul_f32_e32 v68, 0x42000000, v68
	v_mul_f32_e32 v69, 0x42000000, v69
	v_mul_f32_e32 v70, 0x42000000, v70
	v_mul_f32_e32 v71, 0x42000000, v71
	v_mul_f32_e32 v72, 0x42000000, v72
	v_mul_f32_e32 v73, 0x42000000, v73
	v_mul_f32_e32 v74, 0x42000000, v74
	v_mul_f32_e32 v75, 0x42000000, v75
	v_mul_f32_e32 v76, 0x42000000, v76
	v_mul_f32_e32 v77, 0x42000000, v77
	v_mul_f32_e32 v78, 0x42000000, v78
	v_mul_f32_e32 v79, 0x42000000, v79
	v_mul_f32_e32 v80, 0x42000000, v80
	v_mul_f32_e32 v81, 0x42000000, v81
	v_cvt_pk_fp8_f32 v162, v66, v67
	v_cvt_pk_fp8_f32 v163, v70, v71
	v_cvt_pk_fp8_f32 v164, v74, v75
	v_cvt_pk_fp8_f32 v165, v78, v79
	v_cvt_pk_fp8_f32 v162, v68, v69 op_sel:[0,0,1]
	v_cvt_pk_fp8_f32 v163, v72, v73 op_sel:[0,0,1]
	v_cvt_pk_fp8_f32 v164, v76, v77 op_sel:[0,0,1]
	v_cvt_pk_fp8_f32 v165, v80, v81 op_sel:[0,0,1]
	s_waitcnt vmcnt(0)
	v_mul_f32_e32 v82, 0x42000000, v82
	v_mul_f32_e32 v83, 0x42000000, v83
	v_mul_f32_e32 v84, 0x42000000, v84
	v_mul_f32_e32 v85, 0x42000000, v85
	v_mul_f32_e32 v86, 0x42000000, v86
	v_mul_f32_e32 v87, 0x42000000, v87
	v_mul_f32_e32 v88, 0x42000000, v88
	v_mul_f32_e32 v89, 0x42000000, v89
	v_mul_f32_e32 v90, 0x42000000, v90
	v_mul_f32_e32 v91, 0x42000000, v91
	v_mul_f32_e32 v92, 0x42000000, v92
	v_mul_f32_e32 v93, 0x42000000, v93
	v_mul_f32_e32 v94, 0x42000000, v94
	v_mul_f32_e32 v95, 0x42000000, v95
	v_mul_f32_e32 v96, 0x42000000, v96
	v_mul_f32_e32 v97, 0x42000000, v97
	v_cvt_pk_fp8_f32 v166, v82, v83
	v_cvt_pk_fp8_f32 v167, v86, v87
	v_cvt_pk_fp8_f32 v168, v90, v91
	v_cvt_pk_fp8_f32 v169, v94, v95
	v_cvt_pk_fp8_f32 v166, v84, v85 op_sel:[0,0,1]
	v_cvt_pk_fp8_f32 v167, v88, v89 op_sel:[0,0,1]
	v_cvt_pk_fp8_f32 v168, v92, v93 op_sel:[0,0,1]
	v_cvt_pk_fp8_f32 v169, v96, v97 op_sel:[0,0,1]
	s_mov_b32 vcc_lo, 0xaaaaaaaa
	s_mov_b32 vcc_hi, 0xaaaaaaaa
	s_nop 1
	v_cndmask_b32_dpp v170, v154, v158, vcc quad_perm:[1,0,3,2] row_mask:0xf bank_mask:0xf
	v_cndmask_b32_dpp v174, v162, v166, vcc quad_perm:[1,0,3,2] row_mask:0xf bank_mask:0xf
	v_cndmask_b32_dpp v171, v155, v159, vcc quad_perm:[1,0,3,2] row_mask:0xf bank_mask:0xf
	v_cndmask_b32_dpp v175, v163, v167, vcc quad_perm:[1,0,3,2] row_mask:0xf bank_mask:0xf
	v_cndmask_b32_dpp v172, v156, v160, vcc quad_perm:[1,0,3,2] row_mask:0xf bank_mask:0xf
	v_cndmask_b32_dpp v176, v164, v168, vcc quad_perm:[1,0,3,2] row_mask:0xf bank_mask:0xf
	v_cndmask_b32_dpp v173, v157, v161, vcc quad_perm:[1,0,3,2] row_mask:0xf bank_mask:0xf
	v_cndmask_b32_dpp v177, v165, v169, vcc quad_perm:[1,0,3,2] row_mask:0xf bank_mask:0xf
	s_mov_b32 vcc_lo, 0x55555555
	s_mov_b32 vcc_hi, 0x55555555
	s_nop 1
	v_cndmask_b32_dpp v154, v158, v154, vcc quad_perm:[1,0,3,2] row_mask:0xf bank_mask:0xf
	v_cndmask_b32_dpp v162, v166, v162, vcc quad_perm:[1,0,3,2] row_mask:0xf bank_mask:0xf
	v_cndmask_b32_dpp v155, v159, v155, vcc quad_perm:[1,0,3,2] row_mask:0xf bank_mask:0xf
	v_cndmask_b32_dpp v163, v167, v163, vcc quad_perm:[1,0,3,2] row_mask:0xf bank_mask:0xf
	v_cndmask_b32_dpp v156, v160, v156, vcc quad_perm:[1,0,3,2] row_mask:0xf bank_mask:0xf
	v_cndmask_b32_dpp v164, v168, v164, vcc quad_perm:[1,0,3,2] row_mask:0xf bank_mask:0xf
	v_cndmask_b32_dpp v157, v161, v157, vcc quad_perm:[1,0,3,2] row_mask:0xf bank_mask:0xf
	v_cndmask_b32_dpp v165, v169, v165, vcc quad_perm:[1,0,3,2] row_mask:0xf bank_mask:0xf
	s_mov_b32 vcc_lo, 0xcccccccc
	s_mov_b32 vcc_hi, 0xcccccccc
	s_nop 1
	v_cndmask_b32_dpp v158, v154, v162, vcc quad_perm:[2,3,0,1] row_mask:0xf bank_mask:0xf
	v_cndmask_b32_dpp v166, v170, v174, vcc quad_perm:[2,3,0,1] row_mask:0xf bank_mask:0xf
	v_cndmask_b32_dpp v159, v155, v163, vcc quad_perm:[2,3,0,1] row_mask:0xf bank_mask:0xf
	v_cndmask_b32_dpp v167, v171, v175, vcc quad_perm:[2,3,0,1] row_mask:0xf bank_mask:0xf
	v_cndmask_b32_dpp v160, v156, v164, vcc quad_perm:[2,3,0,1] row_mask:0xf bank_mask:0xf
	v_cndmask_b32_dpp v168, v172, v176, vcc quad_perm:[2,3,0,1] row_mask:0xf bank_mask:0xf
	v_cndmask_b32_dpp v161, v157, v165, vcc quad_perm:[2,3,0,1] row_mask:0xf bank_mask:0xf
	v_cndmask_b32_dpp v169, v173, v177, vcc quad_perm:[2,3,0,1] row_mask:0xf bank_mask:0xf
	s_mov_b32 vcc_lo, 0x33333333
	s_mov_b32 vcc_hi, 0x33333333
	s_nop 1
	v_cndmask_b32_dpp v154, v162, v154, vcc quad_perm:[2,3,0,1] row_mask:0xf bank_mask:0xf
	v_cndmask_b32_dpp v170, v174, v170, vcc quad_perm:[2,3,0,1] row_mask:0xf bank_mask:0xf
	v_cndmask_b32_dpp v155, v163, v155, vcc quad_perm:[2,3,0,1] row_mask:0xf bank_mask:0xf
	v_cndmask_b32_dpp v171, v175, v171, vcc quad_perm:[2,3,0,1] row_mask:0xf bank_mask:0xf
	v_cndmask_b32_dpp v156, v164, v156, vcc quad_perm:[2,3,0,1] row_mask:0xf bank_mask:0xf
	v_cndmask_b32_dpp v172, v176, v172, vcc quad_perm:[2,3,0,1] row_mask:0xf bank_mask:0xf
	v_cndmask_b32_dpp v157, v165, v157, vcc quad_perm:[2,3,0,1] row_mask:0xf bank_mask:0xf
	v_cndmask_b32_dpp v173, v177, v173, vcc quad_perm:[2,3,0,1] row_mask:0xf bank_mask:0xf
	global_store_dwordx4 v179, v[154:157], s[82:83] nt
	global_store_dwordx4 v180, v[170:173], s[82:83] nt
	global_store_dwordx4 v181, v[158:161], s[82:83] nt
	global_store_dwordx4 v190, v[166:169], s[82:83] nt
	v_readlane_b32 s2, v239, 0
	s_lshr_b32 s2, s2, 6
	s_sub_i32 s2, s2, 1
	s_mul_i32 s2, s2, 2
	s_add_i32 s2, s2, 1
	s_cmp_gt_u32 s2, 13
	s_cbranch_scc1 .Lhw_seam3_done
	v_readlane_b32 s9, v239, 23
	s_lshr_b32 s9, s9, 3
	s_mul_i32 s9, s9, 14
	s_add_i32 s2, s2, s9
	s_mul_i32 s9, s74, 42
	s_add_i32 s2, s2, s9
	s_cmp_gt_u32 s2, 24575
	s_cbranch_scc1 .Lhw_seam3_done
	v_mbcnt_lo_u32_b32 v178, -1, 0
	v_mbcnt_hi_u32_b32 v178, -1, v178
	v_and_b32_e32 v179, 60, v178
	v_lshlrev_b32_e32 v179, 10, v179
	v_and_b32_e32 v180, 3, v178
	v_lshl_or_b32 v179, v180, 4, v179
	v_add_u32_e32 v180, 0x400, v179
	v_add_u32_e32 v181, 0x800, v179
	v_add_u32_e32 v190, 0xc00, v179
	v_lshlrev_b32_e32 v178, 2, v178
	s_cmp_lt_u32 s2, 16384
	s_cbranch_scc0 .Lhw_dn_s3_1
	s_lshr_b32 s9, s2, 9
	s_bfe_u32 s32, s2, 0x40005
	s_and_b32 s53, s2, 31
	s_lshl_b32 s69, s9, 23
	s_lshl_b32 s100, s32, 19
	s_add_i32 s69, s69, s100
	s_lshl_b32 s100, s53, 8
	s_add_i32 s69, s69, s100
	s_lshl_b32 s98, s9, 11
	s_bfe_u32 s100, s53, 0x30001
	s_lshl_b32 s100, s100, 8
	s_add_i32 s98, s98, s100
	s_lshr_b32 s100, s53, 4
	s_lshl_b32 s100, s100, 7
	s_add_i32 s98, s98, s100
	s_and_b32 s100, s53, 1
	s_lshl_b32 s100, s100, 6
	s_add_i32 s98, s98, s100
	s_lshl_b32 s98, s98, 10
	s_lshl_b32 s100, s32, 6
	s_add_i32 s98, s98, s100
	s_add_i32 s98, s98, 0x2000000
	v_readlane_b32 s82, v239, 11
	v_readlane_b32 s83, v239, 12
	s_movk_i32 s89, 8192
	s_branch .Lhw_go_s3_1

.Lhw_seam4:
	s_mov_b64 exec, -1
	v_readlane_b32 s2, v239, 0
	s_lshr_b32 s2, s2, 6
	s_sub_i32 s2, s2, 1
	s_mul_i32 s2, s2, 2
	s_add_i32 s2, s2, 0
	s_cmp_gt_u32 s2, 13
	s_cbranch_scc1 .Lhw_seam4_done
	v_readlane_b32 s9, v239, 23
	s_lshr_b32 s9, s9, 3
	s_mul_i32 s9, s9, 14
	s_add_i32 s2, s2, s9
	s_mul_i32 s9, s74, 56
	s_add_i32 s2, s2, s9
	s_cmp_gt_u32 s2, 24575
	s_cbranch_scc1 .Lhw_seam4_done
	v_mbcnt_lo_u32_b32 v178, -1, 0
	v_mbcnt_hi_u32_b32 v178, -1, v178
	v_and_b32_e32 v179, 60, v178
	v_lshlrev_b32_e32 v179, 10, v179
	v_and_b32_e32 v180, 3, v178
	v_lshl_or_b32 v179, v180, 4, v179
	v_add_u32_e32 v180, 0x400, v179
	v_add_u32_e32 v181, 0x800, v179
	v_add_u32_e32 v190, 0xc00, v179
	v_lshlrev_b32_e32 v178, 2, v178
	s_cmp_lt_u32 s2, 16384
	s_cbranch_scc0 .Lhw_dn_s4_0
	s_lshr_b32 s9, s2, 9
	s_bfe_u32 s32, s2, 0x40005
	s_and_b32 s53, s2, 31
	s_lshl_b32 s69, s9, 23
	s_lshl_b32 s100, s32, 19
	s_add_i32 s69, s69, s100
	s_lshl_b32 s100, s53, 8
	s_add_i32 s69, s69, s100
	s_lshl_b32 s98, s9, 11
	s_bfe_u32 s100, s53, 0x30001
	s_lshl_b32 s100, s100, 8
	s_add_i32 s98, s98, s100
	s_lshr_b32 s100, s53, 4
	s_lshl_b32 s100, s100, 7
	s_add_i32 s98, s98, s100
	s_and_b32 s100, s53, 1
	s_lshl_b32 s100, s100, 6
	s_add_i32 s98, s98, s100
	s_lshl_b32 s98, s98, 10
	s_lshl_b32 s100, s32, 6
	s_add_i32 s98, s98, s100
	s_add_i32 s98, s98, 0x2000000
	v_readlane_b32 s82, v239, 11
	v_readlane_b32 s83, v239, 12
	s_movk_i32 s89, 8192
	s_branch .Lhw_go_s4_0

.Lhw_go_s4_0:
	s_add_u32 s100, s82, s69
	s_addc_u32 s101, s83, 0
	v_readlane_b32 s82, v239, 44
	v_readlane_b32 s83, v239, 45
	s_add_u32 s82, s82, s98
	s_addc_u32 s83, s83, 0
	global_load_dword v34, v178, s[100:101] nt
	s_add_u32 s100, s100, s89
	s_addc_u32 s101, s101, 0
	global_load_dword v35, v178, s[100:101] nt
	s_add_u32 s100, s100, s89
	s_addc_u32 s101, s101, 0
	global_load_dword v36, v178, s[100:101] nt
	s_add_u32 s100, s100, s89
	s_addc_u32 s101, s101, 0
	global_load_dword v37, v178, s[100:101] nt
	s_add_u32 s100, s100, s89
	s_addc_u32 s101, s101, 0
	global_load_dword v38, v178, s[100:101] nt
	s_add_u32 s100, s100, s89
	s_addc_u32 s101, s101, 0
	global_load_dword v39, v178, s[100:101] nt
	s_add_u32 s100, s100, s89
	s_addc_u32 s101, s101, 0
	global_load_dword v40, v178, s[100:101] nt
	s_add_u32 s100, s100, s89
	s_addc_u32 s101, s101, 0
	global_load_dword v41, v178, s[100:101] nt
	s_add_u32 s100, s100, s89
	s_addc_u32 s101, s101, 0
	global_load_dword v42, v178, s[100:101] nt
	s_add_u32 s100, s100, s89
	s_addc_u32 s101, s101, 0
	global_load_dword v43, v178, s[100:101] nt
	s_add_u32 s100, s100, s89
	s_addc_u32 s101, s101, 0
	global_load_dword v44, v178, s[100:101] nt
	s_add_u32 s100, s100, s89
	s_addc_u32 s101, s101, 0
	global_load_dword v45, v178, s[100:101] nt
	s_add_u32 s100, s100, s89
	s_addc_u32 s101, s101, 0
	global_load_dword v46, v178, s[100:101] nt
	s_add_u32 s100, s100, s89
	s_addc_u32 s101, s101, 0
	global_load_dword v47, v178, s[100:101] nt
	s_add_u32 s100, s100, s89
	s_addc_u32 s101, s101, 0
	global_load_dword v48, v178, s[100:101] nt
	s_add_u32 s100, s100, s89
	s_addc_u32 s101, s101, 0
	global_load_dword v49, v178, s[100:101] nt
	s_add_u32 s100, s100, s89
	s_addc_u32 s101, s101, 0
	global_load_dword v50, v178, s[100:101] nt
	s_add_u32 s100, s100, s89
	s_addc_u32 s101, s101, 0
	global_load_dword v51, v178, s[100:101] nt
	s_add_u32 s100, s100, s89
	s_addc_u32 s101, s101, 0
	global_load_dword v52, v178, s[100:101] nt
	s_add_u32 s100, s100, s89
	s_addc_u32 s101, s101, 0
	global_load_dword v53, v178, s[100:101] nt
	s_add_u32 s100, s100, s89
	s_addc_u32 s101, s101, 0
	global_load_dword v54, v178, s[100:101] nt
	s_add_u32 s100, s100, s89
	s_addc_u32 s101, s101, 0
	global_load_dword v55, v178, s[100:101] nt
	s_add_u32 s100, s100, s89
	s_addc_u32 s101, s101, 0
	global_load_dword v56, v178, s[100:101] nt
	s_add_u32 s100, s100, s89
	s_addc_u32 s101, s101, 0
	global_load_dword v57, v178, s[100:101] nt
	s_add_u32 s100, s100, s89
	s_addc_u32 s101, s101, 0
	global_load_dword v58, v178, s[100:101] nt
	s_add_u32 s100, s100, s89
	s_addc_u32 s101, s101, 0
	global_load_dword v59, v178, s[100:101] nt
	s_add_u32 s100, s100, s89
	s_addc_u32 s101, s101, 0
	global_load_dword v60, v178, s[100:101] nt
	s_add_u32 s100, s100, s89
	s_addc_u32 s101, s101, 0
	global_load_dword v61, v178, s[100:101] nt
	s_add_u32 s100, s100, s89
	s_addc_u32 s101, s101, 0
	global_load_dword v62, v178, s[100:101] nt
	s_add_u32 s100, s100, s89
	s_addc_u32 s101, s101, 0
	global_load_dword v63, v178, s[100:101] nt
	s_add_u32 s100, s100, s89
	s_addc_u32 s101, s101, 0
	global_load_dword v64, v178, s[100:101] nt
	s_add_u32 s100, s100, s89
	s_addc_u32 s101, s101, 0
	global_load_dword v65, v178, s[100:101] nt
	s_add_u32 s100, s100, s89
	s_addc_u32 s101, s101, 0
	global_load_dword v66, v178, s[100:101] nt
	s_add_u32 s100, s100, s89
	s_addc_u32 s101, s101, 0
	global_load_dword v67, v178, s[100:101] nt
	s_add_u32 s100, s100, s89
	s_addc_u32 s101, s101, 0
	global_load_dword v68, v178, s[100:101] nt
	s_add_u32 s100, s100, s89
	s_addc_u32 s101, s101, 0
	global_load_dword v69, v178, s[100:101] nt
	s_add_u32 s100, s100, s89
	s_addc_u32 s101, s101, 0
	global_load_dword v70, v178, s[100:101] nt
	s_add_u32 s100, s100, s89
	s_addc_u32 s101, s101, 0
	global_load_dword v71, v178, s[100:101] nt
	s_add_u32 s100, s100, s89
	s_addc_u32 s101, s101, 0
	global_load_dword v72, v178, s[100:101] nt
	s_add_u32 s100, s100, s89
	s_addc_u32 s101, s101, 0
	global_load_dword v73, v178, s[100:101] nt
	s_add_u32 s100, s100, s89
	s_addc_u32 s101, s101, 0
	global_load_dword v74, v178, s[100:101] nt
	s_add_u32 s100, s100, s89
	s_addc_u32 s101, s101, 0
	global_load_dword v75, v178, s[100:101] nt
	s_add_u32 s100, s100, s89
	s_addc_u32 s101, s101, 0
	global_load_dword v76, v178, s[100:101] nt
	s_add_u32 s100, s100, s89
	s_addc_u32 s101, s101, 0
	global_load_dword v77, v178, s[100:101] nt
	s_add_u32 s100, s100, s89
	s_addc_u32 s101, s101, 0
	global_load_dword v78, v178, s[100:101] nt
	s_add_u32 s100, s100, s89
	s_addc_u32 s101, s101, 0
	global_load_dword v79, v178, s[100:101] nt
	s_add_u32 s100, s100, s89
	s_addc_u32 s101, s101, 0
	global_load_dword v80, v178, s[100:101] nt
	s_add_u32 s100, s100, s89
	s_addc_u32 s101, s101, 0
	global_load_dword v81, v178, s[100:101] nt
	s_add_u32 s100, s100, s89
	s_addc_u32 s101, s101, 0
	global_load_dword v82, v178, s[100:101] nt
	s_add_u32 s100, s100, s89
	s_addc_u32 s101, s101, 0
	global_load_dword v83, v178, s[100:101] nt
	s_add_u32 s100, s100, s89
	s_addc_u32 s101, s101, 0
	global_load_dword v84, v178, s[100:101] nt
	s_add_u32 s100, s100, s89
	s_addc_u32 s101, s101, 0
	global_load_dword v85, v178, s[100:101] nt
	s_add_u32 s100, s100, s89
	s_addc_u32 s101, s101, 0
	global_load_dword v86, v178, s[100:101] nt
	s_add_u32 s100, s100, s89
	s_addc_u32 s101, s101, 0
	global_load_dword v87, v178, s[100:101] nt
	s_add_u32 s100, s100, s89
	s_addc_u32 s101, s101, 0
	global_load_dword v88, v178, s[100:101] nt
	s_add_u32 s100, s100, s89
	s_addc_u32 s101, s101, 0
	global_load_dword v89, v178, s[100:101] nt
	s_add_u32 s100, s100, s89
	s_addc_u32 s101, s101, 0
	global_load_dword v90, v178, s[100:101] nt
	s_add_u32 s100, s100, s89
	s_addc_u32 s101, s101, 0
	global_load_dword v91, v178, s[100:101] nt
	s_add_u32 s100, s100, s89
	s_addc_u32 s101, s101, 0
	global_load_dword v92, v178, s[100:101] nt
	s_add_u32 s100, s100, s89
	s_addc_u32 s101, s101, 0
	global_load_dword v93, v178, s[100:101] nt
	s_add_u32 s100, s100, s89
	s_addc_u32 s101, s101, 0
	global_load_dword v94, v178, s[100:101] nt
	s_add_u32 s100, s100, s89
	s_addc_u32 s101, s101, 0
	global_load_dword v95, v178, s[100:101] nt
	s_add_u32 s100, s100, s89
	s_addc_u32 s101, s101, 0
	global_load_dword v96, v178, s[100:101] nt
	s_add_u32 s100, s100, s89
	s_addc_u32 s101, s101, 0
	global_load_dword v97, v178, s[100:101] nt
	s_add_u32 s100, s100, s89
	s_addc_u32 s101, s101, 0
	s_waitcnt vmcnt(48)
	v_mul_f32_e32 v34, 0x42000000, v34
	v_mul_f32_e32 v35, 0x42000000, v35
	v_mul_f32_e32 v36, 0x42000000, v36
	v_mul_f32_e32 v37, 0x42000000, v37
	v_mul_f32_e32 v38, 0x42000000, v38
	v_mul_f32_e32 v39, 0x42000000, v39
	v_mul_f32_e32 v40, 0x42000000, v40
	v_mul_f32_e32 v41, 0x42000000, v41
	v_mul_f32_e32 v42, 0x42000000, v42
	v_mul_f32_e32 v43, 0x42000000, v43
	v_mul_f32_e32 v44, 0x42000000, v44
	v_mul_f32_e32 v45, 0x42000000, v45
	v_mul_f32_e32 v46, 0x42000000, v46
	v_mul_f32_e32 v47, 0x42000000, v47
	v_mul_f32_e32 v48, 0x42000000, v48
	v_mul_f32_e32 v49, 0x42000000, v49
	v_cvt_pk_fp8_f32 v154, v34, v35
	v_cvt_pk_fp8_f32 v155, v38, v39
	v_cvt_pk_fp8_f32 v156, v42, v43
	v_cvt_pk_fp8_f32 v157, v46, v47
	v_cvt_pk_fp8_f32 v154, v36, v37 op_sel:[0,0,1]
	v_cvt_pk_fp8_f32 v155, v40, v41 op_sel:[0,0,1]
	v_cvt_pk_fp8_f32 v156, v44, v45 op_sel:[0,0,1]
	v_cvt_pk_fp8_f32 v157, v48, v49 op_sel:[0,0,1]
	s_waitcnt vmcnt(32)
	v_mul_f32_e32 v50, 0x42000000, v50
	v_mul_f32_e32 v51, 0x42000000, v51
	v_mul_f32_e32 v52, 0x42000000, v52
	v_mul_f32_e32 v53, 0x42000000, v53
	v_mul_f32_e32 v54, 0x42000000, v54
	v_mul_f32_e32 v55, 0x42000000, v55
	v_mul_f32_e32 v56, 0x42000000, v56
	v_mul_f32_e32 v57, 0x42000000, v57
	v_mul_f32_e32 v58, 0x42000000, v58
	v_mul_f32_e32 v59, 0x42000000, v59
	v_mul_f32_e32 v60, 0x42000000, v60
	v_mul_f32_e32 v61, 0x42000000, v61
	v_mul_f32_e32 v62, 0x42000000, v62
	v_mul_f32_e32 v63, 0x42000000, v63
	v_mul_f32_e32 v64, 0x42000000, v64
	v_mul_f32_e32 v65, 0x42000000, v65
	v_cvt_pk_fp8_f32 v158, v50, v51
	v_cvt_pk_fp8_f32 v159, v54, v55
	v_cvt_pk_fp8_f32 v160, v58, v59
	v_cvt_pk_fp8_f32 v161, v62, v63
	v_cvt_pk_fp8_f32 v158, v52, v53 op_sel:[0,0,1]
	v_cvt_pk_fp8_f32 v159, v56, v57 op_sel:[0,0,1]
	v_cvt_pk_fp8_f32 v160, v60, v61 op_sel:[0,0,1]
	v_cvt_pk_fp8_f32 v161, v64, v65 op_sel:[0,0,1]
	s_waitcnt vmcnt(16)
	v_mul_f32_e32 v66, 0x42000000, v66
	v_mul_f32_e32 v67, 0x42000000, v67
	v_mul_f32_e32 v68, 0x42000000, v68
	v_mul_f32_e32 v69, 0x42000000, v69
	v_mul_f32_e32 v70, 0x42000000, v70
	v_mul_f32_e32 v71, 0x42000000, v71
	v_mul_f32_e32 v72, 0x42000000, v72
	v_mul_f32_e32 v73, 0x42000000, v73
	v_mul_f32_e32 v74, 0x42000000, v74
	v_mul_f32_e32 v75, 0x42000000, v75
	v_mul_f32_e32 v76, 0x42000000, v76
	v_mul_f32_e32 v77, 0x42000000, v77
	v_mul_f32_e32 v78, 0x42000000, v78
	v_mul_f32_e32 v79, 0x42000000, v79
	v_mul_f32_e32 v80, 0x42000000, v80
	v_mul_f32_e32 v81, 0x42000000, v81
	v_cvt_pk_fp8_f32 v162, v66, v67
	v_cvt_pk_fp8_f32 v163, v70, v71
	v_cvt_pk_fp8_f32 v164, v74, v75
	v_cvt_pk_fp8_f32 v165, v78, v79
	v_cvt_pk_fp8_f32 v162, v68, v69 op_sel:[0,0,1]
	v_cvt_pk_fp8_f32 v163, v72, v73 op_sel:[0,0,1]
	v_cvt_pk_fp8_f32 v164, v76, v77 op_sel:[0,0,1]
	v_cvt_pk_fp8_f32 v165, v80, v81 op_sel:[0,0,1]
	s_waitcnt vmcnt(0)
	v_mul_f32_e32 v82, 0x42000000, v82
	v_mul_f32_e32 v83, 0x42000000, v83
	v_mul_f32_e32 v84, 0x42000000, v84
	v_mul_f32_e32 v85, 0x42000000, v85
	v_mul_f32_e32 v86, 0x42000000, v86
	v_mul_f32_e32 v87, 0x42000000, v87
	v_mul_f32_e32 v88, 0x42000000, v88
	v_mul_f32_e32 v89, 0x42000000, v89
	v_mul_f32_e32 v90, 0x42000000, v90
	v_mul_f32_e32 v91, 0x42000000, v91
	v_mul_f32_e32 v92, 0x42000000, v92
	v_mul_f32_e32 v93, 0x42000000, v93
	v_mul_f32_e32 v94, 0x42000000, v94
	v_mul_f32_e32 v95, 0x42000000, v95
	v_mul_f32_e32 v96, 0x42000000, v96
	v_mul_f32_e32 v97, 0x42000000, v97
	v_cvt_pk_fp8_f32 v166, v82, v83
	v_cvt_pk_fp8_f32 v167, v86, v87
	v_cvt_pk_fp8_f32 v168, v90, v91
	v_cvt_pk_fp8_f32 v169, v94, v95
	v_cvt_pk_fp8_f32 v166, v84, v85 op_sel:[0,0,1]
	v_cvt_pk_fp8_f32 v167, v88, v89 op_sel:[0,0,1]
	v_cvt_pk_fp8_f32 v168, v92, v93 op_sel:[0,0,1]
	v_cvt_pk_fp8_f32 v169, v96, v97 op_sel:[0,0,1]
	s_mov_b32 vcc_lo, 0xaaaaaaaa
	s_mov_b32 vcc_hi, 0xaaaaaaaa
	s_nop 1
	v_cndmask_b32_dpp v170, v154, v158, vcc quad_perm:[1,0,3,2] row_mask:0xf bank_mask:0xf
	v_cndmask_b32_dpp v174, v162, v166, vcc quad_perm:[1,0,3,2] row_mask:0xf bank_mask:0xf
	v_cndmask_b32_dpp v171, v155, v159, vcc quad_perm:[1,0,3,2] row_mask:0xf bank_mask:0xf
	v_cndmask_b32_dpp v175, v163, v167, vcc quad_perm:[1,0,3,2] row_mask:0xf bank_mask:0xf
	v_cndmask_b32_dpp v172, v156, v160, vcc quad_perm:[1,0,3,2] row_mask:0xf bank_mask:0xf
	v_cndmask_b32_dpp v176, v164, v168, vcc quad_perm:[1,0,3,2] row_mask:0xf bank_mask:0xf
	v_cndmask_b32_dpp v173, v157, v161, vcc quad_perm:[1,0,3,2] row_mask:0xf bank_mask:0xf
	v_cndmask_b32_dpp v177, v165, v169, vcc quad_perm:[1,0,3,2] row_mask:0xf bank_mask:0xf
	s_mov_b32 vcc_lo, 0x55555555
	s_mov_b32 vcc_hi, 0x55555555
	s_nop 1
	v_cndmask_b32_dpp v154, v158, v154, vcc quad_perm:[1,0,3,2] row_mask:0xf bank_mask:0xf
	v_cndmask_b32_dpp v162, v166, v162, vcc quad_perm:[1,0,3,2] row_mask:0xf bank_mask:0xf
	v_cndmask_b32_dpp v155, v159, v155, vcc quad_perm:[1,0,3,2] row_mask:0xf bank_mask:0xf
	v_cndmask_b32_dpp v163, v167, v163, vcc quad_perm:[1,0,3,2] row_mask:0xf bank_mask:0xf
	v_cndmask_b32_dpp v156, v160, v156, vcc quad_perm:[1,0,3,2] row_mask:0xf bank_mask:0xf
	v_cndmask_b32_dpp v164, v168, v164, vcc quad_perm:[1,0,3,2] row_mask:0xf bank_mask:0xf
	v_cndmask_b32_dpp v157, v161, v157, vcc quad_perm:[1,0,3,2] row_mask:0xf bank_mask:0xf
	v_cndmask_b32_dpp v165, v169, v165, vcc quad_perm:[1,0,3,2] row_mask:0xf bank_mask:0xf
	s_mov_b32 vcc_lo, 0xcccccccc
	s_mov_b32 vcc_hi, 0xcccccccc
	s_nop 1
	v_cndmask_b32_dpp v158, v154, v162, vcc quad_perm:[2,3,0,1] row_mask:0xf bank_mask:0xf
	v_cndmask_b32_dpp v166, v170, v174, vcc quad_perm:[2,3,0,1] row_mask:0xf bank_mask:0xf
	v_cndmask_b32_dpp v159, v155, v163, vcc quad_perm:[2,3,0,1] row_mask:0xf bank_mask:0xf
	v_cndmask_b32_dpp v167, v171, v175, vcc quad_perm:[2,3,0,1] row_mask:0xf bank_mask:0xf
	v_cndmask_b32_dpp v160, v156, v164, vcc quad_perm:[2,3,0,1] row_mask:0xf bank_mask:0xf
	v_cndmask_b32_dpp v168, v172, v176, vcc quad_perm:[2,3,0,1] row_mask:0xf bank_mask:0xf
	v_cndmask_b32_dpp v161, v157, v165, vcc quad_perm:[2,3,0,1] row_mask:0xf bank_mask:0xf
	v_cndmask_b32_dpp v169, v173, v177, vcc quad_perm:[2,3,0,1] row_mask:0xf bank_mask:0xf
	s_mov_b32 vcc_lo, 0x33333333
	s_mov_b32 vcc_hi, 0x33333333
	s_nop 1
	v_cndmask_b32_dpp v154, v162, v154, vcc quad_perm:[2,3,0,1] row_mask:0xf bank_mask:0xf
	v_cndmask_b32_dpp v170, v174, v170, vcc quad_perm:[2,3,0,1] row_mask:0xf bank_mask:0xf
	v_cndmask_b32_dpp v155, v163, v155, vcc quad_perm:[2,3,0,1] row_mask:0xf bank_mask:0xf
	v_cndmask_b32_dpp v171, v175, v171, vcc quad_perm:[2,3,0,1] row_mask:0xf bank_mask:0xf
	v_cndmask_b32_dpp v156, v164, v156, vcc quad_perm:[2,3,0,1] row_mask:0xf bank_mask:0xf
	v_cndmask_b32_dpp v172, v176, v172, vcc quad_perm:[2,3,0,1] row_mask:0xf bank_mask:0xf
	v_cndmask_b32_dpp v157, v165, v157, vcc quad_perm:[2,3,0,1] row_mask:0xf bank_mask:0xf
	v_cndmask_b32_dpp v173, v177, v173, vcc quad_perm:[2,3,0,1] row_mask:0xf bank_mask:0xf
	global_store_dwordx4 v179, v[154:157], s[82:83] nt
	global_store_dwordx4 v180, v[170:173], s[82:83] nt
	global_store_dwordx4 v181, v[158:161], s[82:83] nt
	global_store_dwordx4 v190, v[166:169], s[82:83] nt
	v_readlane_b32 s2, v239, 0
	s_lshr_b32 s2, s2, 6
	s_sub_i32 s2, s2, 1
	s_mul_i32 s2, s2, 2
	s_add_i32 s2, s2, 1
	s_cmp_gt_u32 s2, 13
	s_cbranch_scc1 .Lhw_seam4_done
	v_readlane_b32 s9, v239, 23
	s_lshr_b32 s9, s9, 3
	s_mul_i32 s9, s9, 14
	s_add_i32 s2, s2, s9
	s_mul_i32 s9, s74, 56
	s_add_i32 s2, s2, s9
	s_cmp_gt_u32 s2, 24575
	s_cbranch_scc1 .Lhw_seam4_done
	v_mbcnt_lo_u32_b32 v178, -1, 0
	v_mbcnt_hi_u32_b32 v178, -1, v178
	v_and_b32_e32 v179, 60, v178
	v_lshlrev_b32_e32 v179, 10, v179
	v_and_b32_e32 v180, 3, v178
	v_lshl_or_b32 v179, v180, 4, v179
	v_add_u32_e32 v180, 0x400, v179
	v_add_u32_e32 v181, 0x800, v179
	v_add_u32_e32 v190, 0xc00, v179
	v_lshlrev_b32_e32 v178, 2, v178
	s_cmp_lt_u32 s2, 16384
	s_cbranch_scc0 .Lhw_dn_s4_1
	s_lshr_b32 s9, s2, 9
	s_bfe_u32 s32, s2, 0x40005
	s_and_b32 s53, s2, 31
	s_lshl_b32 s69, s9, 23
	s_lshl_b32 s100, s32, 19
	s_add_i32 s69, s69, s100
	s_lshl_b32 s100, s53, 8
	s_add_i32 s69, s69, s100
	s_lshl_b32 s98, s9, 11
	s_bfe_u32 s100, s53, 0x30001
	s_lshl_b32 s100, s100, 8
	s_add_i32 s98, s98, s100
	s_lshr_b32 s100, s53, 4
	s_lshl_b32 s100, s100, 7
	s_add_i32 s98, s98, s100
	s_and_b32 s100, s53, 1
	s_lshl_b32 s100, s100, 6
	s_add_i32 s98, s98, s100
	s_lshl_b32 s98, s98, 10
	s_lshl_b32 s100, s32, 6
	s_add_i32 s98, s98, s100
	s_add_i32 s98, s98, 0x2000000
	v_readlane_b32 s82, v239, 11
	v_readlane_b32 s83, v239, 12
	s_movk_i32 s89, 8192
	s_branch .Lhw_go_s4_1

.Lhw_seam5:
	s_mov_b64 exec, -1
	v_readlane_b32 s2, v239, 0
	s_lshr_b32 s2, s2, 6
	s_sub_i32 s2, s2, 1
	s_mul_i32 s2, s2, 2
	s_add_i32 s2, s2, 0
	s_cmp_gt_u32 s2, 13
	s_cbranch_scc1 .Lhw_seam5_done
	v_readlane_b32 s9, v239, 23
	s_lshr_b32 s9, s9, 3
	s_mul_i32 s9, s9, 14
	s_add_i32 s2, s2, s9
	s_mul_i32 s9, s74, 70
	s_add_i32 s2, s2, s9
	s_cmp_gt_u32 s2, 24575
	s_cbranch_scc1 .Lhw_seam5_done
	v_mbcnt_lo_u32_b32 v178, -1, 0
	v_mbcnt_hi_u32_b32 v178, -1, v178
	v_and_b32_e32 v179, 60, v178
	v_lshlrev_b32_e32 v179, 10, v179
	v_and_b32_e32 v180, 3, v178
	v_lshl_or_b32 v179, v180, 4, v179
	v_add_u32_e32 v180, 0x400, v179
	v_add_u32_e32 v181, 0x800, v179
	v_add_u32_e32 v190, 0xc00, v179
	v_lshlrev_b32_e32 v178, 2, v178
	s_cmp_lt_u32 s2, 16384
	s_cbranch_scc0 .Lhw_dn_s5_0
	s_lshr_b32 s9, s2, 9
	s_bfe_u32 s32, s2, 0x40005
	s_and_b32 s53, s2, 31
	s_lshl_b32 s69, s9, 23
	s_lshl_b32 s100, s32, 19
	s_add_i32 s69, s69, s100
	s_lshl_b32 s100, s53, 8
	s_add_i32 s69, s69, s100
	s_lshl_b32 s98, s9, 11
	s_bfe_u32 s100, s53, 0x30001
	s_lshl_b32 s100, s100, 8
	s_add_i32 s98, s98, s100
	s_lshr_b32 s100, s53, 4
	s_lshl_b32 s100, s100, 7
	s_add_i32 s98, s98, s100
	s_and_b32 s100, s53, 1
	s_lshl_b32 s100, s100, 6
	s_add_i32 s98, s98, s100
	s_lshl_b32 s98, s98, 10
	s_lshl_b32 s100, s32, 6
	s_add_i32 s98, s98, s100
	s_add_i32 s98, s98, 0x2000000
	v_readlane_b32 s82, v239, 11
	v_readlane_b32 s83, v239, 12
	s_movk_i32 s89, 8192
	s_branch .Lhw_go_s5_0

.Lhw_go_s5_0:
	s_add_u32 s100, s82, s69
	s_addc_u32 s101, s83, 0
	v_readlane_b32 s82, v239, 44
	v_readlane_b32 s83, v239, 45
	s_add_u32 s82, s82, s98
	s_addc_u32 s83, s83, 0
	global_load_dword v34, v178, s[100:101] nt
	s_add_u32 s100, s100, s89
	s_addc_u32 s101, s101, 0
	global_load_dword v35, v178, s[100:101] nt
	s_add_u32 s100, s100, s89
	s_addc_u32 s101, s101, 0
	global_load_dword v36, v178, s[100:101] nt
	s_add_u32 s100, s100, s89
	s_addc_u32 s101, s101, 0
	global_load_dword v37, v178, s[100:101] nt
	s_add_u32 s100, s100, s89
	s_addc_u32 s101, s101, 0
	global_load_dword v38, v178, s[100:101] nt
	s_add_u32 s100, s100, s89
	s_addc_u32 s101, s101, 0
	global_load_dword v39, v178, s[100:101] nt
	s_add_u32 s100, s100, s89
	s_addc_u32 s101, s101, 0
	global_load_dword v40, v178, s[100:101] nt
	s_add_u32 s100, s100, s89
	s_addc_u32 s101, s101, 0
	global_load_dword v41, v178, s[100:101] nt
	s_add_u32 s100, s100, s89
	s_addc_u32 s101, s101, 0
	global_load_dword v42, v178, s[100:101] nt
	s_add_u32 s100, s100, s89
	s_addc_u32 s101, s101, 0
	global_load_dword v43, v178, s[100:101] nt
	s_add_u32 s100, s100, s89
	s_addc_u32 s101, s101, 0
	global_load_dword v44, v178, s[100:101] nt
	s_add_u32 s100, s100, s89
	s_addc_u32 s101, s101, 0
	global_load_dword v45, v178, s[100:101] nt
	s_add_u32 s100, s100, s89
	s_addc_u32 s101, s101, 0
	global_load_dword v46, v178, s[100:101] nt
	s_add_u32 s100, s100, s89
	s_addc_u32 s101, s101, 0
	global_load_dword v47, v178, s[100:101] nt
	s_add_u32 s100, s100, s89
	s_addc_u32 s101, s101, 0
	global_load_dword v48, v178, s[100:101] nt
	s_add_u32 s100, s100, s89
	s_addc_u32 s101, s101, 0
	global_load_dword v49, v178, s[100:101] nt
	s_add_u32 s100, s100, s89
	s_addc_u32 s101, s101, 0
	global_load_dword v50, v178, s[100:101] nt
	s_add_u32 s100, s100, s89
	s_addc_u32 s101, s101, 0
	global_load_dword v51, v178, s[100:101] nt
	s_add_u32 s100, s100, s89
	s_addc_u32 s101, s101, 0
	global_load_dword v52, v178, s[100:101] nt
	s_add_u32 s100, s100, s89
	s_addc_u32 s101, s101, 0
	global_load_dword v53, v178, s[100:101] nt
	s_add_u32 s100, s100, s89
	s_addc_u32 s101, s101, 0
	global_load_dword v54, v178, s[100:101] nt
	s_add_u32 s100, s100, s89
	s_addc_u32 s101, s101, 0
	global_load_dword v55, v178, s[100:101] nt
	s_add_u32 s100, s100, s89
	s_addc_u32 s101, s101, 0
	global_load_dword v56, v178, s[100:101] nt
	s_add_u32 s100, s100, s89
	s_addc_u32 s101, s101, 0
	global_load_dword v57, v178, s[100:101] nt
	s_add_u32 s100, s100, s89
	s_addc_u32 s101, s101, 0
	global_load_dword v58, v178, s[100:101] nt
	s_add_u32 s100, s100, s89
	s_addc_u32 s101, s101, 0
	global_load_dword v59, v178, s[100:101] nt
	s_add_u32 s100, s100, s89
	s_addc_u32 s101, s101, 0
	global_load_dword v60, v178, s[100:101] nt
	s_add_u32 s100, s100, s89
	s_addc_u32 s101, s101, 0
	global_load_dword v61, v178, s[100:101] nt
	s_add_u32 s100, s100, s89
	s_addc_u32 s101, s101, 0
	global_load_dword v62, v178, s[100:101] nt
	s_add_u32 s100, s100, s89
	s_addc_u32 s101, s101, 0
	global_load_dword v63, v178, s[100:101] nt
	s_add_u32 s100, s100, s89
	s_addc_u32 s101, s101, 0
	global_load_dword v64, v178, s[100:101] nt
	s_add_u32 s100, s100, s89
	s_addc_u32 s101, s101, 0
	global_load_dword v65, v178, s[100:101] nt
	s_add_u32 s100, s100, s89
	s_addc_u32 s101, s101, 0
	global_load_dword v66, v178, s[100:101] nt
	s_add_u32 s100, s100, s89
	s_addc_u32 s101, s101, 0
	global_load_dword v67, v178, s[100:101] nt
	s_add_u32 s100, s100, s89
	s_addc_u32 s101, s101, 0
	global_load_dword v68, v178, s[100:101] nt
	s_add_u32 s100, s100, s89
	s_addc_u32 s101, s101, 0
	global_load_dword v69, v178, s[100:101] nt
	s_add_u32 s100, s100, s89
	s_addc_u32 s101, s101, 0
	global_load_dword v70, v178, s[100:101] nt
	s_add_u32 s100, s100, s89
	s_addc_u32 s101, s101, 0
	global_load_dword v71, v178, s[100:101] nt
	s_add_u32 s100, s100, s89
	s_addc_u32 s101, s101, 0
	global_load_dword v72, v178, s[100:101] nt
	s_add_u32 s100, s100, s89
	s_addc_u32 s101, s101, 0
	global_load_dword v73, v178, s[100:101] nt
	s_add_u32 s100, s100, s89
	s_addc_u32 s101, s101, 0
	global_load_dword v74, v178, s[100:101] nt
	s_add_u32 s100, s100, s89
	s_addc_u32 s101, s101, 0
	global_load_dword v75, v178, s[100:101] nt
	s_add_u32 s100, s100, s89
	s_addc_u32 s101, s101, 0
	global_load_dword v76, v178, s[100:101] nt
	s_add_u32 s100, s100, s89
	s_addc_u32 s101, s101, 0
	global_load_dword v77, v178, s[100:101] nt
	s_add_u32 s100, s100, s89
	s_addc_u32 s101, s101, 0
	global_load_dword v78, v178, s[100:101] nt
	s_add_u32 s100, s100, s89
	s_addc_u32 s101, s101, 0
	global_load_dword v79, v178, s[100:101] nt
	s_add_u32 s100, s100, s89
	s_addc_u32 s101, s101, 0
	global_load_dword v80, v178, s[100:101] nt
	s_add_u32 s100, s100, s89
	s_addc_u32 s101, s101, 0
	global_load_dword v81, v178, s[100:101] nt
	s_add_u32 s100, s100, s89
	s_addc_u32 s101, s101, 0
	global_load_dword v82, v178, s[100:101] nt
	s_add_u32 s100, s100, s89
	s_addc_u32 s101, s101, 0
	global_load_dword v83, v178, s[100:101] nt
	s_add_u32 s100, s100, s89
	s_addc_u32 s101, s101, 0
	global_load_dword v84, v178, s[100:101] nt
	s_add_u32 s100, s100, s89
	s_addc_u32 s101, s101, 0
	global_load_dword v85, v178, s[100:101] nt
	s_add_u32 s100, s100, s89
	s_addc_u32 s101, s101, 0
	global_load_dword v86, v178, s[100:101] nt
	s_add_u32 s100, s100, s89
	s_addc_u32 s101, s101, 0
	global_load_dword v87, v178, s[100:101] nt
	s_add_u32 s100, s100, s89
	s_addc_u32 s101, s101, 0
	global_load_dword v88, v178, s[100:101] nt
	s_add_u32 s100, s100, s89
	s_addc_u32 s101, s101, 0
	global_load_dword v89, v178, s[100:101] nt
	s_add_u32 s100, s100, s89
	s_addc_u32 s101, s101, 0
	global_load_dword v90, v178, s[100:101] nt
	s_add_u32 s100, s100, s89
	s_addc_u32 s101, s101, 0
	global_load_dword v91, v178, s[100:101] nt
	s_add_u32 s100, s100, s89
	s_addc_u32 s101, s101, 0
	global_load_dword v92, v178, s[100:101] nt
	s_add_u32 s100, s100, s89
	s_addc_u32 s101, s101, 0
	global_load_dword v93, v178, s[100:101] nt
	s_add_u32 s100, s100, s89
	s_addc_u32 s101, s101, 0
	global_load_dword v94, v178, s[100:101] nt
	s_add_u32 s100, s100, s89
	s_addc_u32 s101, s101, 0
	global_load_dword v95, v178, s[100:101] nt
	s_add_u32 s100, s100, s89
	s_addc_u32 s101, s101, 0
	global_load_dword v96, v178, s[100:101] nt
	s_add_u32 s100, s100, s89
	s_addc_u32 s101, s101, 0
	global_load_dword v97, v178, s[100:101] nt
	s_add_u32 s100, s100, s89
	s_addc_u32 s101, s101, 0
	s_waitcnt vmcnt(48)
	v_mul_f32_e32 v34, 0x42000000, v34
	v_mul_f32_e32 v35, 0x42000000, v35
	v_mul_f32_e32 v36, 0x42000000, v36
	v_mul_f32_e32 v37, 0x42000000, v37
	v_mul_f32_e32 v38, 0x42000000, v38
	v_mul_f32_e32 v39, 0x42000000, v39
	v_mul_f32_e32 v40, 0x42000000, v40
	v_mul_f32_e32 v41, 0x42000000, v41
	v_mul_f32_e32 v42, 0x42000000, v42
	v_mul_f32_e32 v43, 0x42000000, v43
	v_mul_f32_e32 v44, 0x42000000, v44
	v_mul_f32_e32 v45, 0x42000000, v45
	v_mul_f32_e32 v46, 0x42000000, v46
	v_mul_f32_e32 v47, 0x42000000, v47
	v_mul_f32_e32 v48, 0x42000000, v48
	v_mul_f32_e32 v49, 0x42000000, v49
	v_cvt_pk_fp8_f32 v154, v34, v35
	v_cvt_pk_fp8_f32 v155, v38, v39
	v_cvt_pk_fp8_f32 v156, v42, v43
	v_cvt_pk_fp8_f32 v157, v46, v47
	v_cvt_pk_fp8_f32 v154, v36, v37 op_sel:[0,0,1]
	v_cvt_pk_fp8_f32 v155, v40, v41 op_sel:[0,0,1]
	v_cvt_pk_fp8_f32 v156, v44, v45 op_sel:[0,0,1]
	v_cvt_pk_fp8_f32 v157, v48, v49 op_sel:[0,0,1]
	s_waitcnt vmcnt(32)
	v_mul_f32_e32 v50, 0x42000000, v50
	v_mul_f32_e32 v51, 0x42000000, v51
	v_mul_f32_e32 v52, 0x42000000, v52
	v_mul_f32_e32 v53, 0x42000000, v53
	v_mul_f32_e32 v54, 0x42000000, v54
	v_mul_f32_e32 v55, 0x42000000, v55
	v_mul_f32_e32 v56, 0x42000000, v56
	v_mul_f32_e32 v57, 0x42000000, v57
	v_mul_f32_e32 v58, 0x42000000, v58
	v_mul_f32_e32 v59, 0x42000000, v59
	v_mul_f32_e32 v60, 0x42000000, v60
	v_mul_f32_e32 v61, 0x42000000, v61
	v_mul_f32_e32 v62, 0x42000000, v62
	v_mul_f32_e32 v63, 0x42000000, v63
	v_mul_f32_e32 v64, 0x42000000, v64
	v_mul_f32_e32 v65, 0x42000000, v65
	v_cvt_pk_fp8_f32 v158, v50, v51
	v_cvt_pk_fp8_f32 v159, v54, v55
	v_cvt_pk_fp8_f32 v160, v58, v59
	v_cvt_pk_fp8_f32 v161, v62, v63
	v_cvt_pk_fp8_f32 v158, v52, v53 op_sel:[0,0,1]
	v_cvt_pk_fp8_f32 v159, v56, v57 op_sel:[0,0,1]
	v_cvt_pk_fp8_f32 v160, v60, v61 op_sel:[0,0,1]
	v_cvt_pk_fp8_f32 v161, v64, v65 op_sel:[0,0,1]
	s_waitcnt vmcnt(16)
	v_mul_f32_e32 v66, 0x42000000, v66
	v_mul_f32_e32 v67, 0x42000000, v67
	v_mul_f32_e32 v68, 0x42000000, v68
	v_mul_f32_e32 v69, 0x42000000, v69
	v_mul_f32_e32 v70, 0x42000000, v70
	v_mul_f32_e32 v71, 0x42000000, v71
	v_mul_f32_e32 v72, 0x42000000, v72
	v_mul_f32_e32 v73, 0x42000000, v73
	v_mul_f32_e32 v74, 0x42000000, v74
	v_mul_f32_e32 v75, 0x42000000, v75
	v_mul_f32_e32 v76, 0x42000000, v76
	v_mul_f32_e32 v77, 0x42000000, v77
	v_mul_f32_e32 v78, 0x42000000, v78
	v_mul_f32_e32 v79, 0x42000000, v79
	v_mul_f32_e32 v80, 0x42000000, v80
	v_mul_f32_e32 v81, 0x42000000, v81
	v_cvt_pk_fp8_f32 v162, v66, v67
	v_cvt_pk_fp8_f32 v163, v70, v71
	v_cvt_pk_fp8_f32 v164, v74, v75
	v_cvt_pk_fp8_f32 v165, v78, v79
	v_cvt_pk_fp8_f32 v162, v68, v69 op_sel:[0,0,1]
	v_cvt_pk_fp8_f32 v163, v72, v73 op_sel:[0,0,1]
	v_cvt_pk_fp8_f32 v164, v76, v77 op_sel:[0,0,1]
	v_cvt_pk_fp8_f32 v165, v80, v81 op_sel:[0,0,1]
	s_waitcnt vmcnt(0)
	v_mul_f32_e32 v82, 0x42000000, v82
	v_mul_f32_e32 v83, 0x42000000, v83
	v_mul_f32_e32 v84, 0x42000000, v84
	v_mul_f32_e32 v85, 0x42000000, v85
	v_mul_f32_e32 v86, 0x42000000, v86
	v_mul_f32_e32 v87, 0x42000000, v87
	v_mul_f32_e32 v88, 0x42000000, v88
	v_mul_f32_e32 v89, 0x42000000, v89
	v_mul_f32_e32 v90, 0x42000000, v90
	v_mul_f32_e32 v91, 0x42000000, v91
	v_mul_f32_e32 v92, 0x42000000, v92
	v_mul_f32_e32 v93, 0x42000000, v93
	v_mul_f32_e32 v94, 0x42000000, v94
	v_mul_f32_e32 v95, 0x42000000, v95
	v_mul_f32_e32 v96, 0x42000000, v96
	v_mul_f32_e32 v97, 0x42000000, v97
	v_cvt_pk_fp8_f32 v166, v82, v83
	v_cvt_pk_fp8_f32 v167, v86, v87
	v_cvt_pk_fp8_f32 v168, v90, v91
	v_cvt_pk_fp8_f32 v169, v94, v95
	v_cvt_pk_fp8_f32 v166, v84, v85 op_sel:[0,0,1]
	v_cvt_pk_fp8_f32 v167, v88, v89 op_sel:[0,0,1]
	v_cvt_pk_fp8_f32 v168, v92, v93 op_sel:[0,0,1]
	v_cvt_pk_fp8_f32 v169, v96, v97 op_sel:[0,0,1]
	s_mov_b32 vcc_lo, 0xaaaaaaaa
	s_mov_b32 vcc_hi, 0xaaaaaaaa
	s_nop 1
	v_cndmask_b32_dpp v170, v154, v158, vcc quad_perm:[1,0,3,2] row_mask:0xf bank_mask:0xf
	v_cndmask_b32_dpp v174, v162, v166, vcc quad_perm:[1,0,3,2] row_mask:0xf bank_mask:0xf
	v_cndmask_b32_dpp v171, v155, v159, vcc quad_perm:[1,0,3,2] row_mask:0xf bank_mask:0xf
	v_cndmask_b32_dpp v175, v163, v167, vcc quad_perm:[1,0,3,2] row_mask:0xf bank_mask:0xf
	v_cndmask_b32_dpp v172, v156, v160, vcc quad_perm:[1,0,3,2] row_mask:0xf bank_mask:0xf
	v_cndmask_b32_dpp v176, v164, v168, vcc quad_perm:[1,0,3,2] row_mask:0xf bank_mask:0xf
	v_cndmask_b32_dpp v173, v157, v161, vcc quad_perm:[1,0,3,2] row_mask:0xf bank_mask:0xf
	v_cndmask_b32_dpp v177, v165, v169, vcc quad_perm:[1,0,3,2] row_mask:0xf bank_mask:0xf
	s_mov_b32 vcc_lo, 0x55555555
	s_mov_b32 vcc_hi, 0x55555555
	s_nop 1
	v_cndmask_b32_dpp v154, v158, v154, vcc quad_perm:[1,0,3,2] row_mask:0xf bank_mask:0xf
	v_cndmask_b32_dpp v162, v166, v162, vcc quad_perm:[1,0,3,2] row_mask:0xf bank_mask:0xf
	v_cndmask_b32_dpp v155, v159, v155, vcc quad_perm:[1,0,3,2] row_mask:0xf bank_mask:0xf
	v_cndmask_b32_dpp v163, v167, v163, vcc quad_perm:[1,0,3,2] row_mask:0xf bank_mask:0xf
	v_cndmask_b32_dpp v156, v160, v156, vcc quad_perm:[1,0,3,2] row_mask:0xf bank_mask:0xf
	v_cndmask_b32_dpp v164, v168, v164, vcc quad_perm:[1,0,3,2] row_mask:0xf bank_mask:0xf
	v_cndmask_b32_dpp v157, v161, v157, vcc quad_perm:[1,0,3,2] row_mask:0xf bank_mask:0xf
	v_cndmask_b32_dpp v165, v169, v165, vcc quad_perm:[1,0,3,2] row_mask:0xf bank_mask:0xf
	s_mov_b32 vcc_lo, 0xcccccccc
	s_mov_b32 vcc_hi, 0xcccccccc
	s_nop 1
	v_cndmask_b32_dpp v158, v154, v162, vcc quad_perm:[2,3,0,1] row_mask:0xf bank_mask:0xf
	v_cndmask_b32_dpp v166, v170, v174, vcc quad_perm:[2,3,0,1] row_mask:0xf bank_mask:0xf
	v_cndmask_b32_dpp v159, v155, v163, vcc quad_perm:[2,3,0,1] row_mask:0xf bank_mask:0xf
	v_cndmask_b32_dpp v167, v171, v175, vcc quad_perm:[2,3,0,1] row_mask:0xf bank_mask:0xf
	v_cndmask_b32_dpp v160, v156, v164, vcc quad_perm:[2,3,0,1] row_mask:0xf bank_mask:0xf
	v_cndmask_b32_dpp v168, v172, v176, vcc quad_perm:[2,3,0,1] row_mask:0xf bank_mask:0xf
	v_cndmask_b32_dpp v161, v157, v165, vcc quad_perm:[2,3,0,1] row_mask:0xf bank_mask:0xf
	v_cndmask_b32_dpp v169, v173, v177, vcc quad_perm:[2,3,0,1] row_mask:0xf bank_mask:0xf
	s_mov_b32 vcc_lo, 0x33333333
	s_mov_b32 vcc_hi, 0x33333333
	s_nop 1
	v_cndmask_b32_dpp v154, v162, v154, vcc quad_perm:[2,3,0,1] row_mask:0xf bank_mask:0xf
	v_cndmask_b32_dpp v170, v174, v170, vcc quad_perm:[2,3,0,1] row_mask:0xf bank_mask:0xf
	v_cndmask_b32_dpp v155, v163, v155, vcc quad_perm:[2,3,0,1] row_mask:0xf bank_mask:0xf
	v_cndmask_b32_dpp v171, v175, v171, vcc quad_perm:[2,3,0,1] row_mask:0xf bank_mask:0xf
	v_cndmask_b32_dpp v156, v164, v156, vcc quad_perm:[2,3,0,1] row_mask:0xf bank_mask:0xf
	v_cndmask_b32_dpp v172, v176, v172, vcc quad_perm:[2,3,0,1] row_mask:0xf bank_mask:0xf
	v_cndmask_b32_dpp v157, v165, v157, vcc quad_perm:[2,3,0,1] row_mask:0xf bank_mask:0xf
	v_cndmask_b32_dpp v173, v177, v173, vcc quad_perm:[2,3,0,1] row_mask:0xf bank_mask:0xf
	global_store_dwordx4 v179, v[154:157], s[82:83] nt
	global_store_dwordx4 v180, v[170:173], s[82:83] nt
	global_store_dwordx4 v181, v[158:161], s[82:83] nt
	global_store_dwordx4 v190, v[166:169], s[82:83] nt
	v_readlane_b32 s2, v239, 0
	s_lshr_b32 s2, s2, 6
	s_sub_i32 s2, s2, 1
	s_mul_i32 s2, s2, 2
	s_add_i32 s2, s2, 1
	s_cmp_gt_u32 s2, 13
	s_cbranch_scc1 .Lhw_seam5_done
	v_readlane_b32 s9, v239, 23
	s_lshr_b32 s9, s9, 3
	s_mul_i32 s9, s9, 14
	s_add_i32 s2, s2, s9
	s_mul_i32 s9, s74, 70
	s_add_i32 s2, s2, s9
	s_cmp_gt_u32 s2, 24575
	s_cbranch_scc1 .Lhw_seam5_done
	v_mbcnt_lo_u32_b32 v178, -1, 0
	v_mbcnt_hi_u32_b32 v178, -1, v178
	v_and_b32_e32 v179, 60, v178
	v_lshlrev_b32_e32 v179, 10, v179
	v_and_b32_e32 v180, 3, v178
	v_lshl_or_b32 v179, v180, 4, v179
	v_add_u32_e32 v180, 0x400, v179
	v_add_u32_e32 v181, 0x800, v179
	v_add_u32_e32 v190, 0xc00, v179
	v_lshlrev_b32_e32 v178, 2, v178
	s_cmp_lt_u32 s2, 16384
	s_cbranch_scc0 .Lhw_dn_s5_1
	s_lshr_b32 s9, s2, 9
	s_bfe_u32 s32, s2, 0x40005
	s_and_b32 s53, s2, 31
	s_lshl_b32 s69, s9, 23
	s_lshl_b32 s100, s32, 19
	s_add_i32 s69, s69, s100
	s_lshl_b32 s100, s53, 8
	s_add_i32 s69, s69, s100
	s_lshl_b32 s98, s9, 11
	s_bfe_u32 s100, s53, 0x30001
	s_lshl_b32 s100, s100, 8
	s_add_i32 s98, s98, s100
	s_lshr_b32 s100, s53, 4
	s_lshl_b32 s100, s100, 7
	s_add_i32 s98, s98, s100
	s_and_b32 s100, s53, 1
	s_lshl_b32 s100, s100, 6
	s_add_i32 s98, s98, s100
	s_lshl_b32 s98, s98, 10
	s_lshl_b32 s100, s32, 6
	s_add_i32 s98, s98, s100
	s_add_i32 s98, s98, 0x2000000
	v_readlane_b32 s82, v239, 11
	v_readlane_b32 s83, v239, 12
	s_movk_i32 s89, 8192
	s_branch .Lhw_go_s5_1

.Lhw_seam6:
	s_mov_b64 exec, -1
	v_readlane_b32 s2, v239, 0
	s_lshr_b32 s2, s2, 6
	s_sub_i32 s2, s2, 1
	s_mul_i32 s2, s2, 2
	s_add_i32 s2, s2, 0
	s_cmp_gt_u32 s2, 11
	s_cbranch_scc1 .Lhw_seam6_done
	v_readlane_b32 s9, v239, 23
	s_lshr_b32 s9, s9, 3
	s_mul_i32 s9, s9, 12
	s_add_i32 s2, s2, s9
	s_mul_i32 s9, s74, 84
	s_add_i32 s2, s2, s9
	s_cmp_gt_u32 s2, 24575
	s_cbranch_scc1 .Lhw_seam6_done
	v_mbcnt_lo_u32_b32 v178, -1, 0
	v_mbcnt_hi_u32_b32 v178, -1, v178
	v_and_b32_e32 v179, 60, v178
	v_lshlrev_b32_e32 v179, 10, v179
	v_and_b32_e32 v180, 3, v178
	v_lshl_or_b32 v179, v180, 4, v179
	v_add_u32_e32 v180, 0x400, v179
	v_add_u32_e32 v181, 0x800, v179
	v_add_u32_e32 v190, 0xc00, v179
	v_lshlrev_b32_e32 v178, 2, v178
	s_cmp_lt_u32 s2, 16384
	s_cbranch_scc0 .Lhw_dn_s6_0
	s_lshr_b32 s9, s2, 9
	s_bfe_u32 s32, s2, 0x40005
	s_and_b32 s53, s2, 31
	s_lshl_b32 s69, s9, 23
	s_lshl_b32 s100, s32, 19
	s_add_i32 s69, s69, s100
	s_lshl_b32 s100, s53, 8
	s_add_i32 s69, s69, s100
	s_lshl_b32 s98, s9, 11
	s_bfe_u32 s100, s53, 0x30001
	s_lshl_b32 s100, s100, 8
	s_add_i32 s98, s98, s100
	s_lshr_b32 s100, s53, 4
	s_lshl_b32 s100, s100, 7
	s_add_i32 s98, s98, s100
	s_and_b32 s100, s53, 1
	s_lshl_b32 s100, s100, 6
	s_add_i32 s98, s98, s100
	s_lshl_b32 s98, s98, 10
	s_lshl_b32 s100, s32, 6
	s_add_i32 s98, s98, s100
	s_add_i32 s98, s98, 0x2000000
	v_readlane_b32 s82, v239, 11
	v_readlane_b32 s83, v239, 12
	s_movk_i32 s89, 8192
	s_branch .Lhw_go_s6_0

.Lhw_go_s6_0:
	s_add_u32 s100, s82, s69
	s_addc_u32 s101, s83, 0
	v_readlane_b32 s82, v239, 44
	v_readlane_b32 s83, v239, 45
	s_add_u32 s82, s82, s98
	s_addc_u32 s83, s83, 0
	global_load_dword v34, v178, s[100:101] nt
	s_add_u32 s100, s100, s89
	s_addc_u32 s101, s101, 0
	global_load_dword v35, v178, s[100:101] nt
	s_add_u32 s100, s100, s89
	s_addc_u32 s101, s101, 0
	global_load_dword v36, v178, s[100:101] nt
	s_add_u32 s100, s100, s89
	s_addc_u32 s101, s101, 0
	global_load_dword v37, v178, s[100:101] nt
	s_add_u32 s100, s100, s89
	s_addc_u32 s101, s101, 0
	global_load_dword v38, v178, s[100:101] nt
	s_add_u32 s100, s100, s89
	s_addc_u32 s101, s101, 0
	global_load_dword v39, v178, s[100:101] nt
	s_add_u32 s100, s100, s89
	s_addc_u32 s101, s101, 0
	global_load_dword v40, v178, s[100:101] nt
	s_add_u32 s100, s100, s89
	s_addc_u32 s101, s101, 0
	global_load_dword v41, v178, s[100:101] nt
	s_add_u32 s100, s100, s89
	s_addc_u32 s101, s101, 0
	global_load_dword v42, v178, s[100:101] nt
	s_add_u32 s100, s100, s89
	s_addc_u32 s101, s101, 0
	global_load_dword v43, v178, s[100:101] nt
	s_add_u32 s100, s100, s89
	s_addc_u32 s101, s101, 0
	global_load_dword v44, v178, s[100:101] nt
	s_add_u32 s100, s100, s89
	s_addc_u32 s101, s101, 0
	global_load_dword v45, v178, s[100:101] nt
	s_add_u32 s100, s100, s89
	s_addc_u32 s101, s101, 0
	global_load_dword v46, v178, s[100:101] nt
	s_add_u32 s100, s100, s89
	s_addc_u32 s101, s101, 0
	global_load_dword v47, v178, s[100:101] nt
	s_add_u32 s100, s100, s89
	s_addc_u32 s101, s101, 0
	global_load_dword v48, v178, s[100:101] nt
	s_add_u32 s100, s100, s89
	s_addc_u32 s101, s101, 0
	global_load_dword v49, v178, s[100:101] nt
	s_add_u32 s100, s100, s89
	s_addc_u32 s101, s101, 0
	global_load_dword v50, v178, s[100:101] nt
	s_add_u32 s100, s100, s89
	s_addc_u32 s101, s101, 0
	global_load_dword v51, v178, s[100:101] nt
	s_add_u32 s100, s100, s89
	s_addc_u32 s101, s101, 0
	global_load_dword v52, v178, s[100:101] nt
	s_add_u32 s100, s100, s89
	s_addc_u32 s101, s101, 0
	global_load_dword v53, v178, s[100:101] nt
	s_add_u32 s100, s100, s89
	s_addc_u32 s101, s101, 0
	global_load_dword v54, v178, s[100:101] nt
	s_add_u32 s100, s100, s89
	s_addc_u32 s101, s101, 0
	global_load_dword v55, v178, s[100:101] nt
	s_add_u32 s100, s100, s89
	s_addc_u32 s101, s101, 0
	global_load_dword v56, v178, s[100:101] nt
	s_add_u32 s100, s100, s89
	s_addc_u32 s101, s101, 0
	global_load_dword v57, v178, s[100:101] nt
	s_add_u32 s100, s100, s89
	s_addc_u32 s101, s101, 0
	global_load_dword v58, v178, s[100:101] nt
	s_add_u32 s100, s100, s89
	s_addc_u32 s101, s101, 0
	global_load_dword v59, v178, s[100:101] nt
	s_add_u32 s100, s100, s89
	s_addc_u32 s101, s101, 0
	global_load_dword v60, v178, s[100:101] nt
	s_add_u32 s100, s100, s89
	s_addc_u32 s101, s101, 0
	global_load_dword v61, v178, s[100:101] nt
	s_add_u32 s100, s100, s89
	s_addc_u32 s101, s101, 0
	global_load_dword v62, v178, s[100:101] nt
	s_add_u32 s100, s100, s89
	s_addc_u32 s101, s101, 0
	global_load_dword v63, v178, s[100:101] nt
	s_add_u32 s100, s100, s89
	s_addc_u32 s101, s101, 0
	global_load_dword v64, v178, s[100:101] nt
	s_add_u32 s100, s100, s89
	s_addc_u32 s101, s101, 0
	global_load_dword v65, v178, s[100:101] nt
	s_add_u32 s100, s100, s89
	s_addc_u32 s101, s101, 0
	global_load_dword v66, v178, s[100:101] nt
	s_add_u32 s100, s100, s89
	s_addc_u32 s101, s101, 0
	global_load_dword v67, v178, s[100:101] nt
	s_add_u32 s100, s100, s89
	s_addc_u32 s101, s101, 0
	global_load_dword v68, v178, s[100:101] nt
	s_add_u32 s100, s100, s89
	s_addc_u32 s101, s101, 0
	global_load_dword v69, v178, s[100:101] nt
	s_add_u32 s100, s100, s89
	s_addc_u32 s101, s101, 0
	global_load_dword v70, v178, s[100:101] nt
	s_add_u32 s100, s100, s89
	s_addc_u32 s101, s101, 0
	global_load_dword v71, v178, s[100:101] nt
	s_add_u32 s100, s100, s89
	s_addc_u32 s101, s101, 0
	global_load_dword v72, v178, s[100:101] nt
	s_add_u32 s100, s100, s89
	s_addc_u32 s101, s101, 0
	global_load_dword v73, v178, s[100:101] nt
	s_add_u32 s100, s100, s89
	s_addc_u32 s101, s101, 0
	global_load_dword v74, v178, s[100:101] nt
	s_add_u32 s100, s100, s89
	s_addc_u32 s101, s101, 0
	global_load_dword v75, v178, s[100:101] nt
	s_add_u32 s100, s100, s89
	s_addc_u32 s101, s101, 0
	global_load_dword v76, v178, s[100:101] nt
	s_add_u32 s100, s100, s89
	s_addc_u32 s101, s101, 0
	global_load_dword v77, v178, s[100:101] nt
	s_add_u32 s100, s100, s89
	s_addc_u32 s101, s101, 0
	global_load_dword v78, v178, s[100:101] nt
	s_add_u32 s100, s100, s89
	s_addc_u32 s101, s101, 0
	global_load_dword v79, v178, s[100:101] nt
	s_add_u32 s100, s100, s89
	s_addc_u32 s101, s101, 0
	global_load_dword v80, v178, s[100:101] nt
	s_add_u32 s100, s100, s89
	s_addc_u32 s101, s101, 0
	global_load_dword v81, v178, s[100:101] nt
	s_add_u32 s100, s100, s89
	s_addc_u32 s101, s101, 0
	global_load_dword v82, v178, s[100:101] nt
	s_add_u32 s100, s100, s89
	s_addc_u32 s101, s101, 0
	global_load_dword v83, v178, s[100:101] nt
	s_add_u32 s100, s100, s89
	s_addc_u32 s101, s101, 0
	global_load_dword v84, v178, s[100:101] nt
	s_add_u32 s100, s100, s89
	s_addc_u32 s101, s101, 0
	global_load_dword v85, v178, s[100:101] nt
	s_add_u32 s100, s100, s89
	s_addc_u32 s101, s101, 0
	global_load_dword v86, v178, s[100:101] nt
	s_add_u32 s100, s100, s89
	s_addc_u32 s101, s101, 0
	global_load_dword v87, v178, s[100:101] nt
	s_add_u32 s100, s100, s89
	s_addc_u32 s101, s101, 0
	global_load_dword v88, v178, s[100:101] nt
	s_add_u32 s100, s100, s89
	s_addc_u32 s101, s101, 0
	global_load_dword v89, v178, s[100:101] nt
	s_add_u32 s100, s100, s89
	s_addc_u32 s101, s101, 0
	global_load_dword v90, v178, s[100:101] nt
	s_add_u32 s100, s100, s89
	s_addc_u32 s101, s101, 0
	global_load_dword v91, v178, s[100:101] nt
	s_add_u32 s100, s100, s89
	s_addc_u32 s101, s101, 0
	global_load_dword v92, v178, s[100:101] nt
	s_add_u32 s100, s100, s89
	s_addc_u32 s101, s101, 0
	global_load_dword v93, v178, s[100:101] nt
	s_add_u32 s100, s100, s89
	s_addc_u32 s101, s101, 0
	global_load_dword v94, v178, s[100:101] nt
	s_add_u32 s100, s100, s89
	s_addc_u32 s101, s101, 0
	global_load_dword v95, v178, s[100:101] nt
	s_add_u32 s100, s100, s89
	s_addc_u32 s101, s101, 0
	global_load_dword v96, v178, s[100:101] nt
	s_add_u32 s100, s100, s89
	s_addc_u32 s101, s101, 0
	global_load_dword v97, v178, s[100:101] nt
	s_add_u32 s100, s100, s89
	s_addc_u32 s101, s101, 0
	s_waitcnt vmcnt(48)
	v_mul_f32_e32 v34, 0x42000000, v34
	v_mul_f32_e32 v35, 0x42000000, v35
	v_mul_f32_e32 v36, 0x42000000, v36
	v_mul_f32_e32 v37, 0x42000000, v37
	v_mul_f32_e32 v38, 0x42000000, v38
	v_mul_f32_e32 v39, 0x42000000, v39
	v_mul_f32_e32 v40, 0x42000000, v40
	v_mul_f32_e32 v41, 0x42000000, v41
	v_mul_f32_e32 v42, 0x42000000, v42
	v_mul_f32_e32 v43, 0x42000000, v43
	v_mul_f32_e32 v44, 0x42000000, v44
	v_mul_f32_e32 v45, 0x42000000, v45
	v_mul_f32_e32 v46, 0x42000000, v46
	v_mul_f32_e32 v47, 0x42000000, v47
	v_mul_f32_e32 v48, 0x42000000, v48
	v_mul_f32_e32 v49, 0x42000000, v49
	v_cvt_pk_fp8_f32 v154, v34, v35
	v_cvt_pk_fp8_f32 v155, v38, v39
	v_cvt_pk_fp8_f32 v156, v42, v43
	v_cvt_pk_fp8_f32 v157, v46, v47
	v_cvt_pk_fp8_f32 v154, v36, v37 op_sel:[0,0,1]
	v_cvt_pk_fp8_f32 v155, v40, v41 op_sel:[0,0,1]
	v_cvt_pk_fp8_f32 v156, v44, v45 op_sel:[0,0,1]
	v_cvt_pk_fp8_f32 v157, v48, v49 op_sel:[0,0,1]
	s_waitcnt vmcnt(32)
	v_mul_f32_e32 v50, 0x42000000, v50
	v_mul_f32_e32 v51, 0x42000000, v51
	v_mul_f32_e32 v52, 0x42000000, v52
	v_mul_f32_e32 v53, 0x42000000, v53
	v_mul_f32_e32 v54, 0x42000000, v54
	v_mul_f32_e32 v55, 0x42000000, v55
	v_mul_f32_e32 v56, 0x42000000, v56
	v_mul_f32_e32 v57, 0x42000000, v57
	v_mul_f32_e32 v58, 0x42000000, v58
	v_mul_f32_e32 v59, 0x42000000, v59
	v_mul_f32_e32 v60, 0x42000000, v60
	v_mul_f32_e32 v61, 0x42000000, v61
	v_mul_f32_e32 v62, 0x42000000, v62
	v_mul_f32_e32 v63, 0x42000000, v63
	v_mul_f32_e32 v64, 0x42000000, v64
	v_mul_f32_e32 v65, 0x42000000, v65
	v_cvt_pk_fp8_f32 v158, v50, v51
	v_cvt_pk_fp8_f32 v159, v54, v55
	v_cvt_pk_fp8_f32 v160, v58, v59
	v_cvt_pk_fp8_f32 v161, v62, v63
	v_cvt_pk_fp8_f32 v158, v52, v53 op_sel:[0,0,1]
	v_cvt_pk_fp8_f32 v159, v56, v57 op_sel:[0,0,1]
	v_cvt_pk_fp8_f32 v160, v60, v61 op_sel:[0,0,1]
	v_cvt_pk_fp8_f32 v161, v64, v65 op_sel:[0,0,1]
	s_waitcnt vmcnt(16)
	v_mul_f32_e32 v66, 0x42000000, v66
	v_mul_f32_e32 v67, 0x42000000, v67
	v_mul_f32_e32 v68, 0x42000000, v68
	v_mul_f32_e32 v69, 0x42000000, v69
	v_mul_f32_e32 v70, 0x42000000, v70
	v_mul_f32_e32 v71, 0x42000000, v71
	v_mul_f32_e32 v72, 0x42000000, v72
	v_mul_f32_e32 v73, 0x42000000, v73
	v_mul_f32_e32 v74, 0x42000000, v74
	v_mul_f32_e32 v75, 0x42000000, v75
	v_mul_f32_e32 v76, 0x42000000, v76
	v_mul_f32_e32 v77, 0x42000000, v77
	v_mul_f32_e32 v78, 0x42000000, v78
	v_mul_f32_e32 v79, 0x42000000, v79
	v_mul_f32_e32 v80, 0x42000000, v80
	v_mul_f32_e32 v81, 0x42000000, v81
	v_cvt_pk_fp8_f32 v162, v66, v67
	v_cvt_pk_fp8_f32 v163, v70, v71
	v_cvt_pk_fp8_f32 v164, v74, v75
	v_cvt_pk_fp8_f32 v165, v78, v79
	v_cvt_pk_fp8_f32 v162, v68, v69 op_sel:[0,0,1]
	v_cvt_pk_fp8_f32 v163, v72, v73 op_sel:[0,0,1]
	v_cvt_pk_fp8_f32 v164, v76, v77 op_sel:[0,0,1]
	v_cvt_pk_fp8_f32 v165, v80, v81 op_sel:[0,0,1]
	s_waitcnt vmcnt(0)
	v_mul_f32_e32 v82, 0x42000000, v82
	v_mul_f32_e32 v83, 0x42000000, v83
	v_mul_f32_e32 v84, 0x42000000, v84
	v_mul_f32_e32 v85, 0x42000000, v85
	v_mul_f32_e32 v86, 0x42000000, v86
	v_mul_f32_e32 v87, 0x42000000, v87
	v_mul_f32_e32 v88, 0x42000000, v88
	v_mul_f32_e32 v89, 0x42000000, v89
	v_mul_f32_e32 v90, 0x42000000, v90
	v_mul_f32_e32 v91, 0x42000000, v91
	v_mul_f32_e32 v92, 0x42000000, v92
	v_mul_f32_e32 v93, 0x42000000, v93
	v_mul_f32_e32 v94, 0x42000000, v94
	v_mul_f32_e32 v95, 0x42000000, v95
	v_mul_f32_e32 v96, 0x42000000, v96
	v_mul_f32_e32 v97, 0x42000000, v97
	v_cvt_pk_fp8_f32 v166, v82, v83
	v_cvt_pk_fp8_f32 v167, v86, v87
	v_cvt_pk_fp8_f32 v168, v90, v91
	v_cvt_pk_fp8_f32 v169, v94, v95
	v_cvt_pk_fp8_f32 v166, v84, v85 op_sel:[0,0,1]
	v_cvt_pk_fp8_f32 v167, v88, v89 op_sel:[0,0,1]
	v_cvt_pk_fp8_f32 v168, v92, v93 op_sel:[0,0,1]
	v_cvt_pk_fp8_f32 v169, v96, v97 op_sel:[0,0,1]
	s_mov_b32 vcc_lo, 0xaaaaaaaa
	s_mov_b32 vcc_hi, 0xaaaaaaaa
	s_nop 1
	v_cndmask_b32_dpp v170, v154, v158, vcc quad_perm:[1,0,3,2] row_mask:0xf bank_mask:0xf
	v_cndmask_b32_dpp v174, v162, v166, vcc quad_perm:[1,0,3,2] row_mask:0xf bank_mask:0xf
	v_cndmask_b32_dpp v171, v155, v159, vcc quad_perm:[1,0,3,2] row_mask:0xf bank_mask:0xf
	v_cndmask_b32_dpp v175, v163, v167, vcc quad_perm:[1,0,3,2] row_mask:0xf bank_mask:0xf
	v_cndmask_b32_dpp v172, v156, v160, vcc quad_perm:[1,0,3,2] row_mask:0xf bank_mask:0xf
	v_cndmask_b32_dpp v176, v164, v168, vcc quad_perm:[1,0,3,2] row_mask:0xf bank_mask:0xf
	v_cndmask_b32_dpp v173, v157, v161, vcc quad_perm:[1,0,3,2] row_mask:0xf bank_mask:0xf
	v_cndmask_b32_dpp v177, v165, v169, vcc quad_perm:[1,0,3,2] row_mask:0xf bank_mask:0xf
	s_mov_b32 vcc_lo, 0x55555555
	s_mov_b32 vcc_hi, 0x55555555
	s_nop 1
	v_cndmask_b32_dpp v154, v158, v154, vcc quad_perm:[1,0,3,2] row_mask:0xf bank_mask:0xf
	v_cndmask_b32_dpp v162, v166, v162, vcc quad_perm:[1,0,3,2] row_mask:0xf bank_mask:0xf
	v_cndmask_b32_dpp v155, v159, v155, vcc quad_perm:[1,0,3,2] row_mask:0xf bank_mask:0xf
	v_cndmask_b32_dpp v163, v167, v163, vcc quad_perm:[1,0,3,2] row_mask:0xf bank_mask:0xf
	v_cndmask_b32_dpp v156, v160, v156, vcc quad_perm:[1,0,3,2] row_mask:0xf bank_mask:0xf
	v_cndmask_b32_dpp v164, v168, v164, vcc quad_perm:[1,0,3,2] row_mask:0xf bank_mask:0xf
	v_cndmask_b32_dpp v157, v161, v157, vcc quad_perm:[1,0,3,2] row_mask:0xf bank_mask:0xf
	v_cndmask_b32_dpp v165, v169, v165, vcc quad_perm:[1,0,3,2] row_mask:0xf bank_mask:0xf
	s_mov_b32 vcc_lo, 0xcccccccc
	s_mov_b32 vcc_hi, 0xcccccccc
	s_nop 1
	v_cndmask_b32_dpp v158, v154, v162, vcc quad_perm:[2,3,0,1] row_mask:0xf bank_mask:0xf
	v_cndmask_b32_dpp v166, v170, v174, vcc quad_perm:[2,3,0,1] row_mask:0xf bank_mask:0xf
	v_cndmask_b32_dpp v159, v155, v163, vcc quad_perm:[2,3,0,1] row_mask:0xf bank_mask:0xf
	v_cndmask_b32_dpp v167, v171, v175, vcc quad_perm:[2,3,0,1] row_mask:0xf bank_mask:0xf
	v_cndmask_b32_dpp v160, v156, v164, vcc quad_perm:[2,3,0,1] row_mask:0xf bank_mask:0xf
	v_cndmask_b32_dpp v168, v172, v176, vcc quad_perm:[2,3,0,1] row_mask:0xf bank_mask:0xf
	v_cndmask_b32_dpp v161, v157, v165, vcc quad_perm:[2,3,0,1] row_mask:0xf bank_mask:0xf
	v_cndmask_b32_dpp v169, v173, v177, vcc quad_perm:[2,3,0,1] row_mask:0xf bank_mask:0xf
	s_mov_b32 vcc_lo, 0x33333333
	s_mov_b32 vcc_hi, 0x33333333
	s_nop 1
	v_cndmask_b32_dpp v154, v162, v154, vcc quad_perm:[2,3,0,1] row_mask:0xf bank_mask:0xf
	v_cndmask_b32_dpp v170, v174, v170, vcc quad_perm:[2,3,0,1] row_mask:0xf bank_mask:0xf
	v_cndmask_b32_dpp v155, v163, v155, vcc quad_perm:[2,3,0,1] row_mask:0xf bank_mask:0xf
	v_cndmask_b32_dpp v171, v175, v171, vcc quad_perm:[2,3,0,1] row_mask:0xf bank_mask:0xf
	v_cndmask_b32_dpp v156, v164, v156, vcc quad_perm:[2,3,0,1] row_mask:0xf bank_mask:0xf
	v_cndmask_b32_dpp v172, v176, v172, vcc quad_perm:[2,3,0,1] row_mask:0xf bank_mask:0xf
	v_cndmask_b32_dpp v157, v165, v157, vcc quad_perm:[2,3,0,1] row_mask:0xf bank_mask:0xf
	v_cndmask_b32_dpp v173, v177, v173, vcc quad_perm:[2,3,0,1] row_mask:0xf bank_mask:0xf
	global_store_dwordx4 v179, v[154:157], s[82:83] nt
	global_store_dwordx4 v180, v[170:173], s[82:83] nt
	global_store_dwordx4 v181, v[158:161], s[82:83] nt
	global_store_dwordx4 v190, v[166:169], s[82:83] nt
	v_readlane_b32 s2, v239, 0
	s_lshr_b32 s2, s2, 6
	s_sub_i32 s2, s2, 1
	s_mul_i32 s2, s2, 2
	s_add_i32 s2, s2, 1
	s_cmp_gt_u32 s2, 11
	s_cbranch_scc1 .Lhw_seam6_done
	v_readlane_b32 s9, v239, 23
	s_lshr_b32 s9, s9, 3
	s_mul_i32 s9, s9, 12
	s_add_i32 s2, s2, s9
	s_mul_i32 s9, s74, 84
	s_add_i32 s2, s2, s9
	s_cmp_gt_u32 s2, 24575
	s_cbranch_scc1 .Lhw_seam6_done
	v_mbcnt_lo_u32_b32 v178, -1, 0
	v_mbcnt_hi_u32_b32 v178, -1, v178
	v_and_b32_e32 v179, 60, v178
	v_lshlrev_b32_e32 v179, 10, v179
	v_and_b32_e32 v180, 3, v178
	v_lshl_or_b32 v179, v180, 4, v179
	v_add_u32_e32 v180, 0x400, v179
	v_add_u32_e32 v181, 0x800, v179
	v_add_u32_e32 v190, 0xc00, v179
	v_lshlrev_b32_e32 v178, 2, v178
	s_cmp_lt_u32 s2, 16384
	s_cbranch_scc0 .Lhw_dn_s6_1
	s_lshr_b32 s9, s2, 9
	s_bfe_u32 s32, s2, 0x40005
	s_and_b32 s53, s2, 31
	s_lshl_b32 s69, s9, 23
	s_lshl_b32 s100, s32, 19
	s_add_i32 s69, s69, s100
	s_lshl_b32 s100, s53, 8
	s_add_i32 s69, s69, s100
	s_lshl_b32 s98, s9, 11
	s_bfe_u32 s100, s53, 0x30001
	s_lshl_b32 s100, s100, 8
	s_add_i32 s98, s98, s100
	s_lshr_b32 s100, s53, 4
	s_lshl_b32 s100, s100, 7
	s_add_i32 s98, s98, s100
	s_and_b32 s100, s53, 1
	s_lshl_b32 s100, s100, 6
	s_add_i32 s98, s98, s100
	s_lshl_b32 s98, s98, 10
	s_lshl_b32 s100, s32, 6
	s_add_i32 s98, s98, s100
	s_add_i32 s98, s98, 0x2000000
	v_readlane_b32 s82, v239, 11
	v_readlane_b32 s83, v239, 12
	s_movk_i32 s89, 8192
	s_branch .Lhw_go_s6_1
